# back-edge rotation: K-loop counter update and exit test moved above the loop-back barrier in six GEMM loops (on top of v68)
# baseline (speedup 1.0000x reference)
.LBB0_204:
	v_add_u32_e32 v139, 0x10000, v137
	ds_read_b128 v[140:143], v139
	ds_read_b128 v[144:147], v139 offset:1024
	ds_read_b128 v[148:151], v139 offset:2048
	ds_read_b128 v[152:155], v139 offset:3072
	v_add_u32_e32 v139, 0x14000, v137
	ds_read_b128 v[156:159], v139
	ds_read_b128 v[160:163], v139 offset:1024
	ds_read_b128 v[164:167], v139 offset:2048
	ds_read_b128 v[168:171], v139 offset:3072
	s_add_i32 s64, s60, 0xfffc0080
	s_add_i32 s61, s64, s56
	s_cmp_eq_u32 s59, 12
	s_cselect_b64 s[62:63], -1, 0
	s_and_b64 s[14:15], s[62:63], exec
	s_cselect_b32 s61, s58, s61
	s_cselect_b32 s64, 0, s64
	s_add_i32 s14, s57, s60
	s_mov_b32 m0, s45
	ds_read_b128 v[172:175], v138
	ds_read_b128 v[176:179], v138 offset:1024
	ds_read_b128 v[180:183], v138 offset:2048
	ds_read_b128 v[184:187], v138 offset:3072
	ds_read_b128 v[188:191], v138 offset:4096
	ds_read_b128 v[192:195], v138 offset:5120
	ds_read_b128 v[196:199], v138 offset:6144
	ds_read_b128 v[200:203], v138 offset:7168
	buffer_load_dwordx4 v133, s[8:11], s14 offen lds
	s_mov_b32 m0, s47
	s_nop 0
	buffer_load_dwordx4 v135, s[8:11], s14 offen lds
	s_waitcnt vmcnt(8)
	s_waitcnt lgkmcnt(0)
	s_barrier
	s_setprio 1
	s_waitcnt lgkmcnt(7)
	v_mfma_f32_16x16x32_bf16 v[104:107], v[140:143], v[172:175], v[104:107]
	v_mfma_f32_16x16x32_bf16 v[112:115], v[148:151], v[172:175], v[112:115]
	s_waitcnt lgkmcnt(5)
	v_mfma_f32_16x16x32_bf16 v[80:83], v[140:143], v[180:183], v[80:83]
	v_mfma_f32_16x16x32_bf16 v[88:91], v[148:151], v[180:183], v[88:91]
	s_waitcnt lgkmcnt(3)
	v_mfma_f32_16x16x32_bf16 v[40:43], v[140:143], v[188:191], v[40:43]
	v_mfma_f32_16x16x32_bf16 v[52:55], v[148:151], v[188:191], v[52:55]
	s_waitcnt lgkmcnt(1)
	v_mfma_f32_16x16x32_bf16 v[20:23], v[140:143], v[196:199], v[20:23]
	v_mfma_f32_16x16x32_bf16 v[32:35], v[148:151], v[196:199], v[32:35]
	v_mfma_f32_16x16x32_bf16 v[104:107], v[144:147], v[176:179], v[104:107]
	v_mfma_f32_16x16x32_bf16 v[112:115], v[152:155], v[176:179], v[112:115]
	v_mfma_f32_16x16x32_bf16 v[80:83], v[144:147], v[184:187], v[80:83]
	v_mfma_f32_16x16x32_bf16 v[88:91], v[152:155], v[184:187], v[88:91]
	v_mfma_f32_16x16x32_bf16 v[40:43], v[144:147], v[192:195], v[40:43]
	v_mfma_f32_16x16x32_bf16 v[52:55], v[152:155], v[192:195], v[52:55]
	s_waitcnt lgkmcnt(0)
	v_mfma_f32_16x16x32_bf16 v[20:23], v[144:147], v[200:203], v[20:23]
	v_mfma_f32_16x16x32_bf16 v[32:35], v[152:155], v[200:203], v[32:35]
	s_setprio 0
	s_setprio 1
	v_mfma_f32_16x16x32_bf16 v[120:123], v[156:159], v[172:175], v[120:123]
	v_mfma_f32_16x16x32_bf16 v[124:127], v[164:167], v[172:175], v[124:127]
	v_mfma_f32_16x16x32_bf16 v[108:111], v[156:159], v[180:183], v[108:111]
	v_mfma_f32_16x16x32_bf16 v[116:119], v[164:167], v[180:183], v[116:119]
	v_mfma_f32_16x16x32_bf16 v[84:87], v[156:159], v[188:191], v[84:87]
	v_mfma_f32_16x16x32_bf16 v[96:99], v[164:167], v[188:191], v[96:99]
	v_mfma_f32_16x16x32_bf16 v[64:67], v[156:159], v[196:199], v[64:67]
	v_mfma_f32_16x16x32_bf16 v[72:75], v[164:167], v[196:199], v[72:75]
	v_mfma_f32_16x16x32_bf16 v[120:123], v[160:163], v[176:179], v[120:123]
	v_mfma_f32_16x16x32_bf16 v[124:127], v[168:171], v[176:179], v[124:127]
	v_mfma_f32_16x16x32_bf16 v[108:111], v[160:163], v[184:187], v[108:111]
	v_mfma_f32_16x16x32_bf16 v[116:119], v[168:171], v[184:187], v[116:119]
	v_mfma_f32_16x16x32_bf16 v[84:87], v[160:163], v[192:195], v[84:87]
	v_mfma_f32_16x16x32_bf16 v[96:99], v[168:171], v[192:195], v[96:99]
	v_mfma_f32_16x16x32_bf16 v[64:67], v[160:163], v[200:203], v[64:67]
	v_mfma_f32_16x16x32_bf16 v[72:75], v[168:171], v[200:203], v[72:75]
	s_setprio 0
	s_barrier
	s_mov_b32 m0, s26
	s_mov_b32 s14, s10
	s_mov_b32 s15, s11
	ds_read_b128 v[172:175], v138 offset:16384
	ds_read_b128 v[176:179], v138 offset:17408
	ds_read_b128 v[180:183], v138 offset:18432
	ds_read_b128 v[184:187], v138 offset:19456
	ds_read_b128 v[188:191], v138 offset:20480
	ds_read_b128 v[192:195], v138 offset:21504
	ds_read_b128 v[196:199], v138 offset:22528
	ds_read_b128 v[200:203], v138 offset:23552
	buffer_load_dwordx4 v134, s[12:15], s61 offen lds
	s_mov_b32 m0, s27
	s_add_i32 s65, s61, 0x4000
	s_and_b64 s[62:63], s[2:3], s[62:63]
	buffer_load_dwordx4 v136, s[12:15], s61 offen lds
	s_mov_b32 m0, s28
	s_and_b64 s[62:63], s[62:63], exec
	buffer_load_dwordx4 v134, s[12:15], s65 offen lds
	s_mov_b32 m0, s29
	s_cselect_b32 s62, s52, s57
	buffer_load_dwordx4 v136, s[12:15], s65 offen lds
	s_add_i32 s62, s64, s62
	s_mov_b32 m0, s7
	s_nop 0
	buffer_load_dwordx4 v133, s[8:11], s62 offen lds
	s_mov_b32 m0, s30
	s_nop 0
	buffer_load_dwordx4 v135, s[8:11], s62 offen lds
	s_waitcnt vmcnt(8)
	s_waitcnt lgkmcnt(0)
	s_barrier
	s_setprio 1
	s_waitcnt lgkmcnt(7)
	v_mfma_f32_16x16x32_bf16 v[48:51], v[140:143], v[172:175], v[48:51]
	v_mfma_f32_16x16x32_bf16 v[60:63], v[148:151], v[172:175], v[60:63]
	s_waitcnt lgkmcnt(5)
	v_mfma_f32_16x16x32_bf16 v[28:31], v[140:143], v[180:183], v[28:31]
	v_mfma_f32_16x16x32_bf16 v[36:39], v[148:151], v[180:183], v[36:39]
	s_waitcnt lgkmcnt(3)
	v_mfma_f32_16x16x32_bf16 v[8:11], v[140:143], v[188:191], v[8:11]
	v_mfma_f32_16x16x32_bf16 v[12:15], v[148:151], v[188:191], v[12:15]
	s_waitcnt lgkmcnt(1)
	v_mfma_f32_16x16x32_bf16 v[0:3], v[140:143], v[196:199], v[0:3]
	v_mfma_f32_16x16x32_bf16 v[4:7], v[148:151], v[196:199], v[4:7]
	v_mfma_f32_16x16x32_bf16 v[48:51], v[144:147], v[176:179], v[48:51]
	v_mfma_f32_16x16x32_bf16 v[60:63], v[152:155], v[176:179], v[60:63]
	v_mfma_f32_16x16x32_bf16 v[28:31], v[144:147], v[184:187], v[28:31]
	v_mfma_f32_16x16x32_bf16 v[36:39], v[152:155], v[184:187], v[36:39]
	v_mfma_f32_16x16x32_bf16 v[8:11], v[144:147], v[192:195], v[8:11]
	v_mfma_f32_16x16x32_bf16 v[12:15], v[152:155], v[192:195], v[12:15]
	s_waitcnt lgkmcnt(0)
	v_mfma_f32_16x16x32_bf16 v[0:3], v[144:147], v[200:203], v[0:3]
	v_mfma_f32_16x16x32_bf16 v[4:7], v[152:155], v[200:203], v[4:7]
	s_setprio 0
	s_setprio 1
	v_mfma_f32_16x16x32_bf16 v[92:95], v[156:159], v[172:175], v[92:95]
	v_mfma_f32_16x16x32_bf16 v[100:103], v[164:167], v[172:175], v[100:103]
	v_mfma_f32_16x16x32_bf16 v[68:71], v[156:159], v[180:183], v[68:71]
	v_mfma_f32_16x16x32_bf16 v[76:79], v[164:167], v[180:183], v[76:79]
	v_mfma_f32_16x16x32_bf16 v[44:47], v[156:159], v[188:191], v[44:47]
	v_mfma_f32_16x16x32_bf16 v[56:59], v[164:167], v[188:191], v[56:59]
	v_mfma_f32_16x16x32_bf16 v[24:27], v[156:159], v[196:199], v[24:27]
	v_mfma_f32_16x16x32_bf16 v[16:19], v[164:167], v[196:199], v[16:19]
	v_mfma_f32_16x16x32_bf16 v[92:95], v[160:163], v[176:179], v[92:95]
	v_mfma_f32_16x16x32_bf16 v[100:103], v[168:171], v[176:179], v[100:103]
	v_mfma_f32_16x16x32_bf16 v[68:71], v[160:163], v[184:187], v[68:71]
	v_mfma_f32_16x16x32_bf16 v[76:79], v[168:171], v[184:187], v[76:79]
	v_mfma_f32_16x16x32_bf16 v[44:47], v[160:163], v[192:195], v[44:47]
	v_mfma_f32_16x16x32_bf16 v[56:59], v[168:171], v[192:195], v[56:59]
	v_mfma_f32_16x16x32_bf16 v[24:27], v[160:163], v[200:203], v[24:27]
	v_mfma_f32_16x16x32_bf16 v[16:19], v[168:171], v[200:203], v[16:19]
	s_setprio 0
	s_barrier
	v_add_u32_e32 v139, 0x18000, v137
	ds_read_b128 v[140:143], v139
	ds_read_b128 v[144:147], v139 offset:1024
	ds_read_b128 v[148:151], v139 offset:2048
	ds_read_b128 v[152:155], v139 offset:3072
	v_add_u32_e32 v139, 0x1c000, v137
	ds_read_b128 v[156:159], v139
	ds_read_b128 v[160:163], v139 offset:1024
	ds_read_b128 v[164:167], v139 offset:2048
	ds_read_b128 v[168:171], v139 offset:3072
	s_add_i32 s63, s62, 0x40000
	s_mov_b32 m0, s31
	ds_read_b128 v[172:175], v138 offset:32768
	ds_read_b128 v[176:179], v138 offset:33792
	ds_read_b128 v[180:183], v138 offset:34816
	ds_read_b128 v[184:187], v138 offset:35840
	ds_read_b128 v[188:191], v138 offset:36864
	ds_read_b128 v[192:195], v138 offset:37888
	ds_read_b128 v[196:199], v138 offset:38912
	ds_read_b128 v[200:203], v138 offset:39936
	buffer_load_dwordx4 v133, s[8:11], s63 offen lds
	s_mov_b32 m0, s33
	s_nop 0
	buffer_load_dwordx4 v135, s[8:11], s63 offen lds
	s_waitcnt vmcnt(8)
	s_waitcnt lgkmcnt(0)
	s_barrier
	s_setprio 1
	s_waitcnt lgkmcnt(7)
	v_mfma_f32_16x16x32_bf16 v[104:107], v[140:143], v[172:175], v[104:107]
	v_mfma_f32_16x16x32_bf16 v[112:115], v[148:151], v[172:175], v[112:115]
	s_waitcnt lgkmcnt(5)
	v_mfma_f32_16x16x32_bf16 v[80:83], v[140:143], v[180:183], v[80:83]
	v_mfma_f32_16x16x32_bf16 v[88:91], v[148:151], v[180:183], v[88:91]
	s_waitcnt lgkmcnt(3)
	v_mfma_f32_16x16x32_bf16 v[40:43], v[140:143], v[188:191], v[40:43]
	v_mfma_f32_16x16x32_bf16 v[52:55], v[148:151], v[188:191], v[52:55]
	s_waitcnt lgkmcnt(1)
	v_mfma_f32_16x16x32_bf16 v[20:23], v[140:143], v[196:199], v[20:23]
	v_mfma_f32_16x16x32_bf16 v[32:35], v[148:151], v[196:199], v[32:35]
	v_mfma_f32_16x16x32_bf16 v[104:107], v[144:147], v[176:179], v[104:107]
	v_mfma_f32_16x16x32_bf16 v[112:115], v[152:155], v[176:179], v[112:115]
	v_mfma_f32_16x16x32_bf16 v[80:83], v[144:147], v[184:187], v[80:83]
	v_mfma_f32_16x16x32_bf16 v[88:91], v[152:155], v[184:187], v[88:91]
	v_mfma_f32_16x16x32_bf16 v[40:43], v[144:147], v[192:195], v[40:43]
	v_mfma_f32_16x16x32_bf16 v[52:55], v[152:155], v[192:195], v[52:55]
	s_waitcnt lgkmcnt(0)
	v_mfma_f32_16x16x32_bf16 v[20:23], v[144:147], v[200:203], v[20:23]
	v_mfma_f32_16x16x32_bf16 v[32:35], v[152:155], v[200:203], v[32:35]
	s_setprio 0
	s_setprio 1
	v_mfma_f32_16x16x32_bf16 v[120:123], v[156:159], v[172:175], v[120:123]
	v_mfma_f32_16x16x32_bf16 v[124:127], v[164:167], v[172:175], v[124:127]
	v_mfma_f32_16x16x32_bf16 v[108:111], v[156:159], v[180:183], v[108:111]
	v_mfma_f32_16x16x32_bf16 v[116:119], v[164:167], v[180:183], v[116:119]
	v_mfma_f32_16x16x32_bf16 v[84:87], v[156:159], v[188:191], v[84:87]
	v_mfma_f32_16x16x32_bf16 v[96:99], v[164:167], v[188:191], v[96:99]
	v_mfma_f32_16x16x32_bf16 v[64:67], v[156:159], v[196:199], v[64:67]
	v_mfma_f32_16x16x32_bf16 v[72:75], v[164:167], v[196:199], v[72:75]
	v_mfma_f32_16x16x32_bf16 v[120:123], v[160:163], v[176:179], v[120:123]
	v_mfma_f32_16x16x32_bf16 v[124:127], v[168:171], v[176:179], v[124:127]
	v_mfma_f32_16x16x32_bf16 v[108:111], v[160:163], v[184:187], v[108:111]
	v_mfma_f32_16x16x32_bf16 v[116:119], v[168:171], v[184:187], v[116:119]
	v_mfma_f32_16x16x32_bf16 v[84:87], v[160:163], v[192:195], v[84:87]
	v_mfma_f32_16x16x32_bf16 v[96:99], v[168:171], v[192:195], v[96:99]
	v_mfma_f32_16x16x32_bf16 v[64:67], v[160:163], v[200:203], v[64:67]
	v_mfma_f32_16x16x32_bf16 v[72:75], v[168:171], v[200:203], v[72:75]
	s_setprio 0
	s_barrier
	s_mov_b32 m0, s35
	s_or_b32 s63, s61, 0x80
	ds_read_b128 v[172:175], v138 offset:49152
	ds_read_b128 v[176:179], v138 offset:50176
	ds_read_b128 v[180:183], v138 offset:51200
	ds_read_b128 v[184:187], v138 offset:52224
	ds_read_b128 v[188:191], v138 offset:53248
	ds_read_b128 v[192:195], v138 offset:54272
	ds_read_b128 v[196:199], v138 offset:55296
	ds_read_b128 v[200:203], v138 offset:56320
	buffer_load_dwordx4 v134, s[12:15], s63 offen lds
	s_mov_b32 m0, s37
	s_addk_i32 s61, 0x4080
	buffer_load_dwordx4 v136, s[12:15], s63 offen lds
	s_mov_b32 m0, s41
	s_addk_i32 s62, 0x80
	buffer_load_dwordx4 v134, s[12:15], s61 offen lds
	s_mov_b32 m0, s42
	s_nop 0
	buffer_load_dwordx4 v136, s[12:15], s61 offen lds
	s_mov_b32 m0, s39
	s_nop 0
	buffer_load_dwordx4 v133, s[8:11], s62 offen lds
	s_mov_b32 m0, s40
	s_nop 0
	buffer_load_dwordx4 v135, s[8:11], s62 offen lds
	s_waitcnt vmcnt(8)
	s_waitcnt lgkmcnt(0)
	s_barrier
	s_setprio 1
	s_waitcnt lgkmcnt(7)
	v_mfma_f32_16x16x32_bf16 v[48:51], v[140:143], v[172:175], v[48:51]
	v_mfma_f32_16x16x32_bf16 v[60:63], v[148:151], v[172:175], v[60:63]
	s_waitcnt lgkmcnt(5)
	v_mfma_f32_16x16x32_bf16 v[28:31], v[140:143], v[180:183], v[28:31]
	v_mfma_f32_16x16x32_bf16 v[36:39], v[148:151], v[180:183], v[36:39]
	s_waitcnt lgkmcnt(3)
	v_mfma_f32_16x16x32_bf16 v[8:11], v[140:143], v[188:191], v[8:11]
	v_mfma_f32_16x16x32_bf16 v[12:15], v[148:151], v[188:191], v[12:15]
	s_waitcnt lgkmcnt(1)
	v_mfma_f32_16x16x32_bf16 v[0:3], v[140:143], v[196:199], v[0:3]
	v_mfma_f32_16x16x32_bf16 v[4:7], v[148:151], v[196:199], v[4:7]
	v_mfma_f32_16x16x32_bf16 v[48:51], v[144:147], v[176:179], v[48:51]
	v_mfma_f32_16x16x32_bf16 v[60:63], v[152:155], v[176:179], v[60:63]
	v_mfma_f32_16x16x32_bf16 v[28:31], v[144:147], v[184:187], v[28:31]
	v_mfma_f32_16x16x32_bf16 v[36:39], v[152:155], v[184:187], v[36:39]
	v_mfma_f32_16x16x32_bf16 v[8:11], v[144:147], v[192:195], v[8:11]
	v_mfma_f32_16x16x32_bf16 v[12:15], v[152:155], v[192:195], v[12:15]
	s_waitcnt lgkmcnt(0)
	v_mfma_f32_16x16x32_bf16 v[0:3], v[144:147], v[200:203], v[0:3]
	v_mfma_f32_16x16x32_bf16 v[4:7], v[152:155], v[200:203], v[4:7]
	s_setprio 0
	s_setprio 1
	v_mfma_f32_16x16x32_bf16 v[92:95], v[156:159], v[172:175], v[92:95]
	v_mfma_f32_16x16x32_bf16 v[100:103], v[164:167], v[172:175], v[100:103]
	v_mfma_f32_16x16x32_bf16 v[68:71], v[156:159], v[180:183], v[68:71]
	v_mfma_f32_16x16x32_bf16 v[76:79], v[164:167], v[180:183], v[76:79]
	v_mfma_f32_16x16x32_bf16 v[44:47], v[156:159], v[188:191], v[44:47]
	v_mfma_f32_16x16x32_bf16 v[56:59], v[164:167], v[188:191], v[56:59]
	v_mfma_f32_16x16x32_bf16 v[24:27], v[156:159], v[196:199], v[24:27]
	v_mfma_f32_16x16x32_bf16 v[16:19], v[164:167], v[196:199], v[16:19]
	v_mfma_f32_16x16x32_bf16 v[92:95], v[160:163], v[176:179], v[92:95]
	v_mfma_f32_16x16x32_bf16 v[100:103], v[168:171], v[176:179], v[100:103]
	v_mfma_f32_16x16x32_bf16 v[68:71], v[160:163], v[184:187], v[68:71]
	v_mfma_f32_16x16x32_bf16 v[76:79], v[168:171], v[184:187], v[76:79]
	v_mfma_f32_16x16x32_bf16 v[44:47], v[160:163], v[192:195], v[44:47]
	v_mfma_f32_16x16x32_bf16 v[56:59], v[168:171], v[192:195], v[56:59]
	v_mfma_f32_16x16x32_bf16 v[24:27], v[160:163], v[200:203], v[24:27]
	v_mfma_f32_16x16x32_bf16 v[16:19], v[168:171], v[200:203], v[16:19]
	s_setprio 0
	s_add_i32 s59, s59, 2
	s_addk_i32 s60, 0x100
	s_cmp_gt_u32 s59, 13
	s_barrier
	s_cbranch_scc0 .LBB0_204
	s_and_b64 vcc, exec, s[24:25]
	s_cbranch_vccz .LBB0_207
	s_barrier

.LBB0_374:
	v_add_u32_e32 v0, 0x10000, v160
	ds_read_b128 v[132:135], v0
	ds_read_b128 v[136:139], v0 offset:1024
	ds_read_b128 v[140:143], v0 offset:2048
	ds_read_b128 v[144:147], v0 offset:3072
	v_add_u32_e32 v0, 0x14000, v160
	ds_read_b128 v[148:151], v0
	ds_read_b128 v[152:155], v0 offset:1024
	ds_read_b128 v[162:165], v0 offset:2048
	ds_read_b128 v[166:169], v0 offset:3072
	s_add_i32 s46, s42, 0xfffc0080
	s_add_i32 s43, s46, s33
	s_cmp_eq_u32 s3, 12
	s_cselect_b64 s[44:45], -1, 0
	s_and_b64 s[14:15], s[44:45], exec
	s_cselect_b32 s43, s2, s43
	s_cselect_b32 s46, 0, s46
	s_add_i32 s14, s40, s42
	s_mov_b32 m0, s67
	ds_read_b128 v[170:173], v161
	ds_read_b128 v[174:177], v161 offset:1024
	ds_read_b128 v[178:181], v161 offset:2048
	ds_read_b128 v[182:185], v161 offset:3072
	ds_read_b128 v[186:189], v161 offset:4096
	ds_read_b128 v[190:193], v161 offset:5120
	ds_read_b128 v[194:197], v161 offset:6144
	ds_read_b128 v[198:201], v161 offset:7168
	buffer_load_dwordx4 v158, s[8:11], s14 offen lds
	s_mov_b32 m0, s77
	s_nop 0
	buffer_load_dwordx4 v159, s[8:11], s14 offen lds
	s_waitcnt vmcnt(8)
	s_waitcnt lgkmcnt(0)
	s_barrier
	s_setprio 1
	s_waitcnt lgkmcnt(7)
	v_mfma_f32_16x16x32_bf16 v[128:131], v[132:135], v[170:173], v[128:131]
	v_mfma_f32_16x16x32_bf16 v[124:127], v[140:143], v[170:173], v[124:127]
	s_waitcnt lgkmcnt(5)
	v_mfma_f32_16x16x32_bf16 v[112:115], v[132:135], v[178:181], v[112:115]
	v_mfma_f32_16x16x32_bf16 v[108:111], v[140:143], v[178:181], v[108:111]
	s_waitcnt lgkmcnt(3)
	v_mfma_f32_16x16x32_bf16 v[96:99], v[132:135], v[186:189], v[96:99]
	v_mfma_f32_16x16x32_bf16 v[92:95], v[140:143], v[186:189], v[92:95]
	s_waitcnt lgkmcnt(1)
	v_mfma_f32_16x16x32_bf16 v[80:83], v[132:135], v[194:197], v[80:83]
	v_mfma_f32_16x16x32_bf16 v[76:79], v[140:143], v[194:197], v[76:79]
	v_mfma_f32_16x16x32_bf16 v[128:131], v[136:139], v[174:177], v[128:131]
	v_mfma_f32_16x16x32_bf16 v[124:127], v[144:147], v[174:177], v[124:127]
	v_mfma_f32_16x16x32_bf16 v[112:115], v[136:139], v[182:185], v[112:115]
	v_mfma_f32_16x16x32_bf16 v[108:111], v[144:147], v[182:185], v[108:111]
	v_mfma_f32_16x16x32_bf16 v[96:99], v[136:139], v[190:193], v[96:99]
	v_mfma_f32_16x16x32_bf16 v[92:95], v[144:147], v[190:193], v[92:95]
	s_waitcnt lgkmcnt(0)
	v_mfma_f32_16x16x32_bf16 v[80:83], v[136:139], v[198:201], v[80:83]
	v_mfma_f32_16x16x32_bf16 v[76:79], v[144:147], v[198:201], v[76:79]
	s_setprio 0
	s_setprio 1
	v_mfma_f32_16x16x32_bf16 v[120:123], v[148:151], v[170:173], v[120:123]
	v_mfma_f32_16x16x32_bf16 v[116:119], v[162:165], v[170:173], v[116:119]
	v_mfma_f32_16x16x32_bf16 v[104:107], v[148:151], v[178:181], v[104:107]
	v_mfma_f32_16x16x32_bf16 v[100:103], v[162:165], v[178:181], v[100:103]
	v_mfma_f32_16x16x32_bf16 v[88:91], v[148:151], v[186:189], v[88:91]
	v_mfma_f32_16x16x32_bf16 v[84:87], v[162:165], v[186:189], v[84:87]
	v_mfma_f32_16x16x32_bf16 v[72:75], v[148:151], v[194:197], v[72:75]
	v_mfma_f32_16x16x32_bf16 v[68:71], v[162:165], v[194:197], v[68:71]
	v_mfma_f32_16x16x32_bf16 v[120:123], v[152:155], v[174:177], v[120:123]
	v_mfma_f32_16x16x32_bf16 v[116:119], v[166:169], v[174:177], v[116:119]
	v_mfma_f32_16x16x32_bf16 v[104:107], v[152:155], v[182:185], v[104:107]
	v_mfma_f32_16x16x32_bf16 v[100:103], v[166:169], v[182:185], v[100:103]
	v_mfma_f32_16x16x32_bf16 v[88:91], v[152:155], v[190:193], v[88:91]
	v_mfma_f32_16x16x32_bf16 v[84:87], v[166:169], v[190:193], v[84:87]
	v_mfma_f32_16x16x32_bf16 v[72:75], v[152:155], v[198:201], v[72:75]
	v_mfma_f32_16x16x32_bf16 v[68:71], v[166:169], v[198:201], v[68:71]
	s_setprio 0
	s_barrier
	s_mov_b32 m0, s39
	s_mov_b32 s14, s10
	s_mov_b32 s15, s11
	ds_read_b128 v[170:173], v161 offset:16384
	ds_read_b128 v[174:177], v161 offset:17408
	ds_read_b128 v[178:181], v161 offset:18432
	ds_read_b128 v[182:185], v161 offset:19456
	ds_read_b128 v[186:189], v161 offset:20480
	ds_read_b128 v[190:193], v161 offset:21504
	ds_read_b128 v[194:197], v161 offset:22528
	ds_read_b128 v[198:201], v161 offset:23552
	buffer_load_dwordx4 v158, s[12:15], s43 offen lds
	s_mov_b32 m0, s41
	s_add_i32 s47, s43, 0x40000
	s_and_b64 s[44:45], s[48:49], s[44:45]
	buffer_load_dwordx4 v159, s[12:15], s43 offen lds
	s_mov_b32 m0, s52
	s_and_b64 s[44:45], s[44:45], exec
	buffer_load_dwordx4 v158, s[12:15], s47 offen lds
	s_mov_b32 m0, s53
	s_cselect_b32 s44, s84, s40
	buffer_load_dwordx4 v159, s[12:15], s47 offen lds
	s_add_i32 s44, s46, s44
	s_mov_b32 m0, s37
	s_nop 0
	buffer_load_dwordx4 v158, s[8:11], s44 offen lds
	s_mov_b32 m0, s54
	s_nop 0
	buffer_load_dwordx4 v159, s[8:11], s44 offen lds
	s_waitcnt vmcnt(8)
	s_waitcnt lgkmcnt(0)
	s_barrier
	s_setprio 1
	s_waitcnt lgkmcnt(7)
	v_mfma_f32_16x16x32_bf16 v[64:67], v[132:135], v[170:173], v[64:67]
	v_mfma_f32_16x16x32_bf16 v[60:63], v[140:143], v[170:173], v[60:63]
	s_waitcnt lgkmcnt(5)
	v_mfma_f32_16x16x32_bf16 v[48:51], v[132:135], v[178:181], v[48:51]
	v_mfma_f32_16x16x32_bf16 v[44:47], v[140:143], v[178:181], v[44:47]
	s_waitcnt lgkmcnt(3)
	v_mfma_f32_16x16x32_bf16 v[32:35], v[132:135], v[186:189], v[32:35]
	v_mfma_f32_16x16x32_bf16 v[28:31], v[140:143], v[186:189], v[28:31]
	s_waitcnt lgkmcnt(1)
	v_mfma_f32_16x16x32_bf16 v[16:19], v[132:135], v[194:197], v[16:19]
	v_mfma_f32_16x16x32_bf16 v[12:15], v[140:143], v[194:197], v[12:15]
	v_mfma_f32_16x16x32_bf16 v[64:67], v[136:139], v[174:177], v[64:67]
	v_mfma_f32_16x16x32_bf16 v[60:63], v[144:147], v[174:177], v[60:63]
	v_mfma_f32_16x16x32_bf16 v[48:51], v[136:139], v[182:185], v[48:51]
	v_mfma_f32_16x16x32_bf16 v[44:47], v[144:147], v[182:185], v[44:47]
	v_mfma_f32_16x16x32_bf16 v[32:35], v[136:139], v[190:193], v[32:35]
	v_mfma_f32_16x16x32_bf16 v[28:31], v[144:147], v[190:193], v[28:31]
	s_waitcnt lgkmcnt(0)
	v_mfma_f32_16x16x32_bf16 v[16:19], v[136:139], v[198:201], v[16:19]
	v_mfma_f32_16x16x32_bf16 v[12:15], v[144:147], v[198:201], v[12:15]
	s_setprio 0
	s_setprio 1
	v_mfma_f32_16x16x32_bf16 v[56:59], v[148:151], v[170:173], v[56:59]
	v_mfma_f32_16x16x32_bf16 v[52:55], v[162:165], v[170:173], v[52:55]
	v_mfma_f32_16x16x32_bf16 v[40:43], v[148:151], v[178:181], v[40:43]
	v_mfma_f32_16x16x32_bf16 v[36:39], v[162:165], v[178:181], v[36:39]
	v_mfma_f32_16x16x32_bf16 v[24:27], v[148:151], v[186:189], v[24:27]
	v_mfma_f32_16x16x32_bf16 v[20:23], v[162:165], v[186:189], v[20:23]
	v_mfma_f32_16x16x32_bf16 v[8:11], v[148:151], v[194:197], v[8:11]
	v_mfma_f32_16x16x32_bf16 v[2:5], v[162:165], v[194:197], v[4:7]
	v_mfma_f32_16x16x32_bf16 v[56:59], v[152:155], v[174:177], v[56:59]
	v_mfma_f32_16x16x32_bf16 v[52:55], v[166:169], v[174:177], v[52:55]
	v_mfma_f32_16x16x32_bf16 v[40:43], v[152:155], v[182:185], v[40:43]
	v_mfma_f32_16x16x32_bf16 v[36:39], v[166:169], v[182:185], v[36:39]
	v_mfma_f32_16x16x32_bf16 v[24:27], v[152:155], v[190:193], v[24:27]
	v_mfma_f32_16x16x32_bf16 v[20:23], v[166:169], v[190:193], v[20:23]
	v_mfma_f32_16x16x32_bf16 v[8:11], v[152:155], v[198:201], v[8:11]
	v_mfma_f32_16x16x32_bf16 v[2:5], v[166:169], v[198:201], v[2:5]
	s_setprio 0
	s_barrier
	v_add_u32_e32 v0, 0x18000, v160
	ds_read_b128 v[132:135], v0
	ds_read_b128 v[136:139], v0 offset:1024
	ds_read_b128 v[140:143], v0 offset:2048
	ds_read_b128 v[144:147], v0 offset:3072
	v_add_u32_e32 v0, 0x1c000, v160
	ds_read_b128 v[148:151], v0
	ds_read_b128 v[152:155], v0 offset:1024
	ds_read_b128 v[162:165], v0 offset:2048
	ds_read_b128 v[166:169], v0 offset:3072
	s_add_i32 s45, s44, 0x40000
	s_mov_b32 m0, s55
	ds_read_b128 v[170:173], v161 offset:32768
	ds_read_b128 v[174:177], v161 offset:33792
	ds_read_b128 v[178:181], v161 offset:34816
	ds_read_b128 v[182:185], v161 offset:35840
	ds_read_b128 v[186:189], v161 offset:36864
	ds_read_b128 v[190:193], v161 offset:37888
	ds_read_b128 v[194:197], v161 offset:38912
	ds_read_b128 v[198:201], v161 offset:39936
	buffer_load_dwordx4 v158, s[8:11], s45 offen lds
	s_mov_b32 m0, s56
	s_nop 0
	buffer_load_dwordx4 v159, s[8:11], s45 offen lds
	s_waitcnt vmcnt(8)
	s_waitcnt lgkmcnt(0)
	s_barrier
	s_setprio 1
	s_waitcnt lgkmcnt(7)
	v_mfma_f32_16x16x32_bf16 v[128:131], v[132:135], v[170:173], v[128:131]
	v_mfma_f32_16x16x32_bf16 v[124:127], v[140:143], v[170:173], v[124:127]
	s_waitcnt lgkmcnt(5)
	v_mfma_f32_16x16x32_bf16 v[112:115], v[132:135], v[178:181], v[112:115]
	v_mfma_f32_16x16x32_bf16 v[108:111], v[140:143], v[178:181], v[108:111]
	s_waitcnt lgkmcnt(3)
	v_mfma_f32_16x16x32_bf16 v[96:99], v[132:135], v[186:189], v[96:99]
	v_mfma_f32_16x16x32_bf16 v[92:95], v[140:143], v[186:189], v[92:95]
	s_waitcnt lgkmcnt(1)
	v_mfma_f32_16x16x32_bf16 v[80:83], v[132:135], v[194:197], v[80:83]
	v_mfma_f32_16x16x32_bf16 v[76:79], v[140:143], v[194:197], v[76:79]
	v_mfma_f32_16x16x32_bf16 v[128:131], v[136:139], v[174:177], v[128:131]
	v_mfma_f32_16x16x32_bf16 v[124:127], v[144:147], v[174:177], v[124:127]
	v_mfma_f32_16x16x32_bf16 v[112:115], v[136:139], v[182:185], v[112:115]
	v_mfma_f32_16x16x32_bf16 v[108:111], v[144:147], v[182:185], v[108:111]
	v_mfma_f32_16x16x32_bf16 v[96:99], v[136:139], v[190:193], v[96:99]
	v_mfma_f32_16x16x32_bf16 v[92:95], v[144:147], v[190:193], v[92:95]
	s_waitcnt lgkmcnt(0)
	v_mfma_f32_16x16x32_bf16 v[80:83], v[136:139], v[198:201], v[80:83]
	v_mfma_f32_16x16x32_bf16 v[76:79], v[144:147], v[198:201], v[76:79]
	s_setprio 0
	s_setprio 1
	v_mfma_f32_16x16x32_bf16 v[120:123], v[148:151], v[170:173], v[120:123]
	v_mfma_f32_16x16x32_bf16 v[116:119], v[162:165], v[170:173], v[116:119]
	v_mfma_f32_16x16x32_bf16 v[104:107], v[148:151], v[178:181], v[104:107]
	v_mfma_f32_16x16x32_bf16 v[100:103], v[162:165], v[178:181], v[100:103]
	v_mfma_f32_16x16x32_bf16 v[88:91], v[148:151], v[186:189], v[88:91]
	v_mfma_f32_16x16x32_bf16 v[84:87], v[162:165], v[186:189], v[84:87]
	v_mfma_f32_16x16x32_bf16 v[72:75], v[148:151], v[194:197], v[72:75]
	v_mfma_f32_16x16x32_bf16 v[68:71], v[162:165], v[194:197], v[68:71]
	v_mfma_f32_16x16x32_bf16 v[120:123], v[152:155], v[174:177], v[120:123]
	v_mfma_f32_16x16x32_bf16 v[116:119], v[166:169], v[174:177], v[116:119]
	v_mfma_f32_16x16x32_bf16 v[104:107], v[152:155], v[182:185], v[104:107]
	v_mfma_f32_16x16x32_bf16 v[100:103], v[166:169], v[182:185], v[100:103]
	v_mfma_f32_16x16x32_bf16 v[88:91], v[152:155], v[190:193], v[88:91]
	v_mfma_f32_16x16x32_bf16 v[84:87], v[166:169], v[190:193], v[84:87]
	v_mfma_f32_16x16x32_bf16 v[72:75], v[152:155], v[198:201], v[72:75]
	v_mfma_f32_16x16x32_bf16 v[68:71], v[166:169], v[198:201], v[68:71]
	s_setprio 0
	s_barrier
	s_mov_b32 m0, s59
	s_or_b32 s45, s43, 0x80
	ds_read_b128 v[170:173], v161 offset:49152
	ds_read_b128 v[174:177], v161 offset:50176
	ds_read_b128 v[178:181], v161 offset:51200
	ds_read_b128 v[182:185], v161 offset:52224
	ds_read_b128 v[186:189], v161 offset:53248
	ds_read_b128 v[190:193], v161 offset:54272
	ds_read_b128 v[194:197], v161 offset:55296
	ds_read_b128 v[198:201], v161 offset:56320
	buffer_load_dwordx4 v158, s[12:15], s45 offen lds
	s_mov_b32 m0, s60
	s_add_i32 s43, s43, 0x40080
	buffer_load_dwordx4 v159, s[12:15], s45 offen lds
	s_mov_b32 m0, s63
	s_addk_i32 s44, 0x80
	buffer_load_dwordx4 v158, s[12:15], s43 offen lds
	s_mov_b32 m0, s64
	s_nop 0
	buffer_load_dwordx4 v159, s[12:15], s43 offen lds
	s_mov_b32 m0, s61
	s_nop 0
	buffer_load_dwordx4 v158, s[8:11], s44 offen lds
	s_mov_b32 m0, s62
	s_nop 0
	buffer_load_dwordx4 v159, s[8:11], s44 offen lds
	s_waitcnt vmcnt(8)
	s_waitcnt lgkmcnt(0)
	s_barrier
	s_setprio 1
	s_waitcnt lgkmcnt(7)
	v_mfma_f32_16x16x32_bf16 v[64:67], v[132:135], v[170:173], v[64:67]
	v_mfma_f32_16x16x32_bf16 v[60:63], v[140:143], v[170:173], v[60:63]
	s_waitcnt lgkmcnt(5)
	v_mfma_f32_16x16x32_bf16 v[48:51], v[132:135], v[178:181], v[48:51]
	v_mfma_f32_16x16x32_bf16 v[44:47], v[140:143], v[178:181], v[44:47]
	s_waitcnt lgkmcnt(3)
	v_mfma_f32_16x16x32_bf16 v[32:35], v[132:135], v[186:189], v[32:35]
	v_mfma_f32_16x16x32_bf16 v[28:31], v[140:143], v[186:189], v[28:31]
	s_waitcnt lgkmcnt(1)
	v_mfma_f32_16x16x32_bf16 v[16:19], v[132:135], v[194:197], v[16:19]
	v_mfma_f32_16x16x32_bf16 v[12:15], v[140:143], v[194:197], v[12:15]
	v_mfma_f32_16x16x32_bf16 v[64:67], v[136:139], v[174:177], v[64:67]
	v_mfma_f32_16x16x32_bf16 v[60:63], v[144:147], v[174:177], v[60:63]
	v_mfma_f32_16x16x32_bf16 v[48:51], v[136:139], v[182:185], v[48:51]
	v_mfma_f32_16x16x32_bf16 v[44:47], v[144:147], v[182:185], v[44:47]
	v_mfma_f32_16x16x32_bf16 v[32:35], v[136:139], v[190:193], v[32:35]
	v_mfma_f32_16x16x32_bf16 v[28:31], v[144:147], v[190:193], v[28:31]
	s_waitcnt lgkmcnt(0)
	v_mfma_f32_16x16x32_bf16 v[16:19], v[136:139], v[198:201], v[16:19]
	v_mfma_f32_16x16x32_bf16 v[12:15], v[144:147], v[198:201], v[12:15]
	s_setprio 0
	s_setprio 1
	v_mfma_f32_16x16x32_bf16 v[56:59], v[148:151], v[170:173], v[56:59]
	v_mfma_f32_16x16x32_bf16 v[52:55], v[162:165], v[170:173], v[52:55]
	v_mfma_f32_16x16x32_bf16 v[40:43], v[148:151], v[178:181], v[40:43]
	v_mfma_f32_16x16x32_bf16 v[36:39], v[162:165], v[178:181], v[36:39]
	v_mfma_f32_16x16x32_bf16 v[24:27], v[148:151], v[186:189], v[24:27]
	v_mfma_f32_16x16x32_bf16 v[20:23], v[162:165], v[186:189], v[20:23]
	v_mfma_f32_16x16x32_bf16 v[6:9], v[148:151], v[194:197], v[8:11]
	v_mfma_f32_16x16x32_bf16 v[2:5], v[162:165], v[194:197], v[2:5]
	v_mfma_f32_16x16x32_bf16 v[56:59], v[152:155], v[174:177], v[56:59]
	v_mfma_f32_16x16x32_bf16 v[52:55], v[166:169], v[174:177], v[52:55]
	v_mfma_f32_16x16x32_bf16 v[40:43], v[152:155], v[182:185], v[40:43]
	v_mfma_f32_16x16x32_bf16 v[36:39], v[166:169], v[182:185], v[36:39]
	v_mfma_f32_16x16x32_bf16 v[24:27], v[152:155], v[190:193], v[24:27]
	v_mfma_f32_16x16x32_bf16 v[20:23], v[166:169], v[190:193], v[20:23]
	v_mfma_f32_16x16x32_bf16 v[8:11], v[152:155], v[198:201], v[6:9]
	v_mfma_f32_16x16x32_bf16 v[4:7], v[166:169], v[198:201], v[2:5]
	s_setprio 0
	s_add_i32 s3, s3, 2
	s_addk_i32 s42, 0x100
	s_cmp_gt_u32 s3, 13
	s_barrier
	s_cbranch_scc0 .LBB0_374
	s_and_b64 vcc, exec, s[30:31]
	s_cbranch_vccz .LBB0_377
	s_barrier

.LBB0_903:
	v_add_u32_e32 v136, 0x10000, v145
	ds_read_b128 v[132:135], v136
	ds_read_b128 v[148:151], v136 offset:1024
	ds_read_b128 v[152:155], v136 offset:2048
	ds_read_b128 v[156:159], v136 offset:3072
	v_add_u32_e32 v136, 0x14000, v145
	ds_read_b128 v[160:163], v136
	ds_read_b128 v[164:167], v136 offset:1024
	ds_read_b128 v[168:171], v136 offset:2048
	ds_read_b128 v[172:175], v136 offset:3072
	s_add_i32 s68, s64, 0xfffc0080
	s_add_i32 s65, s68, s60
	s_cmp_eq_u32 s63, 12
	s_cselect_b64 s[66:67], -1, 0
	s_and_b64 s[14:15], s[66:67], exec
	s_cselect_b32 s65, s62, s65
	s_cselect_b32 s68, 0, s68
	s_add_i32 s14, s61, s64
	s_mov_b32 m0, s40
	ds_read_b128 v[176:179], v146
	ds_read_b128 v[180:183], v146 offset:1024
	ds_read_b128 v[184:187], v146 offset:2048
	ds_read_b128 v[188:191], v146 offset:3072
	ds_read_b128 v[192:195], v146 offset:4096
	ds_read_b128 v[196:199], v146 offset:5120
	ds_read_b128 v[200:203], v146 offset:6144
	ds_read_b128 v[204:207], v146 offset:7168
	buffer_load_dwordx4 v139, s[8:11], s14 offen lds
	s_mov_b32 m0, s45
	s_nop 0
	buffer_load_dwordx4 v141, s[8:11], s14 offen lds
	s_waitcnt vmcnt(8)
	s_waitcnt lgkmcnt(0)
	s_barrier
	s_setprio 1
	s_waitcnt lgkmcnt(7)
	v_mfma_f32_16x16x32_bf16 v[112:115], v[132:135], v[176:179], v[112:115]
	v_mfma_f32_16x16x32_bf16 v[116:119], v[152:155], v[176:179], v[116:119]
	s_waitcnt lgkmcnt(5)
	v_mfma_f32_16x16x32_bf16 v[96:99], v[132:135], v[184:187], v[96:99]
	v_mfma_f32_16x16x32_bf16 v[100:103], v[152:155], v[184:187], v[100:103]
	s_waitcnt lgkmcnt(3)
	v_mfma_f32_16x16x32_bf16 v[80:83], v[132:135], v[192:195], v[80:83]
	v_mfma_f32_16x16x32_bf16 v[84:87], v[152:155], v[192:195], v[84:87]
	s_waitcnt lgkmcnt(1)
	v_mfma_f32_16x16x32_bf16 v[64:67], v[132:135], v[200:203], v[64:67]
	v_mfma_f32_16x16x32_bf16 v[68:71], v[152:155], v[200:203], v[68:71]
	v_mfma_f32_16x16x32_bf16 v[112:115], v[148:151], v[180:183], v[112:115]
	v_mfma_f32_16x16x32_bf16 v[116:119], v[156:159], v[180:183], v[116:119]
	v_mfma_f32_16x16x32_bf16 v[96:99], v[148:151], v[188:191], v[96:99]
	v_mfma_f32_16x16x32_bf16 v[100:103], v[156:159], v[188:191], v[100:103]
	v_mfma_f32_16x16x32_bf16 v[80:83], v[148:151], v[196:199], v[80:83]
	v_mfma_f32_16x16x32_bf16 v[84:87], v[156:159], v[196:199], v[84:87]
	s_waitcnt lgkmcnt(0)
	v_mfma_f32_16x16x32_bf16 v[64:67], v[148:151], v[204:207], v[64:67]
	v_mfma_f32_16x16x32_bf16 v[68:71], v[156:159], v[204:207], v[68:71]
	s_setprio 0
	s_setprio 1
	v_mfma_f32_16x16x32_bf16 v[124:127], v[160:163], v[176:179], v[124:127]
	v_mfma_f32_16x16x32_bf16 v[120:123], v[168:171], v[176:179], v[120:123]
	v_mfma_f32_16x16x32_bf16 v[108:111], v[160:163], v[184:187], v[108:111]
	v_mfma_f32_16x16x32_bf16 v[104:107], v[168:171], v[184:187], v[104:107]
	v_mfma_f32_16x16x32_bf16 v[92:95], v[160:163], v[192:195], v[92:95]
	v_mfma_f32_16x16x32_bf16 v[88:91], v[168:171], v[192:195], v[88:91]
	v_mfma_f32_16x16x32_bf16 v[76:79], v[160:163], v[200:203], v[76:79]
	v_mfma_f32_16x16x32_bf16 v[72:75], v[168:171], v[200:203], v[72:75]
	v_mfma_f32_16x16x32_bf16 v[124:127], v[164:167], v[180:183], v[124:127]
	v_mfma_f32_16x16x32_bf16 v[120:123], v[172:175], v[180:183], v[120:123]
	v_mfma_f32_16x16x32_bf16 v[108:111], v[164:167], v[188:191], v[108:111]
	v_mfma_f32_16x16x32_bf16 v[104:107], v[172:175], v[188:191], v[104:107]
	v_mfma_f32_16x16x32_bf16 v[92:95], v[164:167], v[196:199], v[92:95]
	v_mfma_f32_16x16x32_bf16 v[88:91], v[172:175], v[196:199], v[88:91]
	v_mfma_f32_16x16x32_bf16 v[76:79], v[164:167], v[204:207], v[76:79]
	v_mfma_f32_16x16x32_bf16 v[72:75], v[172:175], v[204:207], v[72:75]
	s_setprio 0
	s_barrier
	s_mov_b32 m0, s35
	s_mov_b32 s14, s10
	s_mov_b32 s15, s11
	ds_read_b128 v[176:179], v146 offset:16384
	ds_read_b128 v[180:183], v146 offset:17408
	ds_read_b128 v[184:187], v146 offset:18432
	ds_read_b128 v[188:191], v146 offset:19456
	ds_read_b128 v[192:195], v146 offset:20480
	ds_read_b128 v[196:199], v146 offset:21504
	ds_read_b128 v[200:203], v146 offset:22528
	ds_read_b128 v[204:207], v146 offset:23552
	buffer_load_dwordx4 v140, s[12:15], s65 offen lds
	s_mov_b32 m0, s37
	s_add_i32 s69, s65, 0x4000
	s_and_b64 s[66:67], s[2:3], s[66:67]
	buffer_load_dwordx4 v142, s[12:15], s65 offen lds
	s_mov_b32 m0, s39
	s_and_b64 s[66:67], s[66:67], exec
	buffer_load_dwordx4 v140, s[12:15], s69 offen lds
	s_mov_b32 m0, s41
	s_cselect_b32 s66, s42, s61
	buffer_load_dwordx4 v142, s[12:15], s69 offen lds
	s_add_i32 s66, s68, s66
	s_mov_b32 m0, s7
	s_nop 0
	buffer_load_dwordx4 v139, s[8:11], s66 offen lds
	s_mov_b32 m0, s48
	s_nop 0
	buffer_load_dwordx4 v141, s[8:11], s66 offen lds
	s_waitcnt vmcnt(8)
	s_waitcnt lgkmcnt(0)
	s_barrier
	s_setprio 1
	s_waitcnt lgkmcnt(7)
	v_mfma_f32_16x16x32_bf16 v[48:51], v[132:135], v[176:179], v[48:51]
	v_mfma_f32_16x16x32_bf16 v[52:55], v[152:155], v[176:179], v[52:55]
	s_waitcnt lgkmcnt(5)
	v_mfma_f32_16x16x32_bf16 v[32:35], v[132:135], v[184:187], v[32:35]
	v_mfma_f32_16x16x32_bf16 v[36:39], v[152:155], v[184:187], v[36:39]
	s_waitcnt lgkmcnt(3)
	v_mfma_f32_16x16x32_bf16 v[16:19], v[132:135], v[192:195], v[16:19]
	v_mfma_f32_16x16x32_bf16 v[20:23], v[152:155], v[192:195], v[20:23]
	s_waitcnt lgkmcnt(1)
	v_mfma_f32_16x16x32_bf16 v[0:3], v[132:135], v[200:203], v[0:3]
	v_mfma_f32_16x16x32_bf16 v[4:7], v[152:155], v[200:203], v[4:7]
	v_mfma_f32_16x16x32_bf16 v[48:51], v[148:151], v[180:183], v[48:51]
	v_mfma_f32_16x16x32_bf16 v[52:55], v[156:159], v[180:183], v[52:55]
	v_mfma_f32_16x16x32_bf16 v[32:35], v[148:151], v[188:191], v[32:35]
	v_mfma_f32_16x16x32_bf16 v[36:39], v[156:159], v[188:191], v[36:39]
	v_mfma_f32_16x16x32_bf16 v[16:19], v[148:151], v[196:199], v[16:19]
	v_mfma_f32_16x16x32_bf16 v[20:23], v[156:159], v[196:199], v[20:23]
	s_waitcnt lgkmcnt(0)
	v_mfma_f32_16x16x32_bf16 v[0:3], v[148:151], v[204:207], v[0:3]
	v_mfma_f32_16x16x32_bf16 v[4:7], v[156:159], v[204:207], v[4:7]
	s_setprio 0
	s_setprio 1
	v_mfma_f32_16x16x32_bf16 v[60:63], v[160:163], v[176:179], v[60:63]
	v_mfma_f32_16x16x32_bf16 v[56:59], v[168:171], v[176:179], v[56:59]
	v_mfma_f32_16x16x32_bf16 v[44:47], v[160:163], v[184:187], v[44:47]
	v_mfma_f32_16x16x32_bf16 v[40:43], v[168:171], v[184:187], v[40:43]
	v_mfma_f32_16x16x32_bf16 v[28:31], v[160:163], v[192:195], v[28:31]
	v_mfma_f32_16x16x32_bf16 v[24:27], v[168:171], v[192:195], v[24:27]
	v_mfma_f32_16x16x32_bf16 v[12:15], v[160:163], v[200:203], v[12:15]
	v_mfma_f32_16x16x32_bf16 v[8:11], v[168:171], v[200:203], v[8:11]
	v_mfma_f32_16x16x32_bf16 v[60:63], v[164:167], v[180:183], v[60:63]
	v_mfma_f32_16x16x32_bf16 v[56:59], v[172:175], v[180:183], v[56:59]
	v_mfma_f32_16x16x32_bf16 v[44:47], v[164:167], v[188:191], v[44:47]
	v_mfma_f32_16x16x32_bf16 v[40:43], v[172:175], v[188:191], v[40:43]
	v_mfma_f32_16x16x32_bf16 v[28:31], v[164:167], v[196:199], v[28:31]
	v_mfma_f32_16x16x32_bf16 v[24:27], v[172:175], v[196:199], v[24:27]
	v_mfma_f32_16x16x32_bf16 v[12:15], v[164:167], v[204:207], v[12:15]
	v_mfma_f32_16x16x32_bf16 v[8:11], v[172:175], v[204:207], v[8:11]
	s_setprio 0
	s_barrier
	v_add_u32_e32 v136, 0x18000, v145
	ds_read_b128 v[132:135], v136
	ds_read_b128 v[148:151], v136 offset:1024
	ds_read_b128 v[152:155], v136 offset:2048
	ds_read_b128 v[156:159], v136 offset:3072
	v_add_u32_e32 v136, 0x1c000, v145
	ds_read_b128 v[160:163], v136
	ds_read_b128 v[164:167], v136 offset:1024
	ds_read_b128 v[168:171], v136 offset:2048
	ds_read_b128 v[172:175], v136 offset:3072
	s_add_i32 s67, s66, 0x40000
	s_mov_b32 m0, s49
	ds_read_b128 v[176:179], v146 offset:32768
	ds_read_b128 v[180:183], v146 offset:33792
	ds_read_b128 v[184:187], v146 offset:34816
	ds_read_b128 v[188:191], v146 offset:35840
	ds_read_b128 v[192:195], v146 offset:36864
	ds_read_b128 v[196:199], v146 offset:37888
	ds_read_b128 v[200:203], v146 offset:38912
	ds_read_b128 v[204:207], v146 offset:39936
	buffer_load_dwordx4 v139, s[8:11], s67 offen lds
	s_mov_b32 m0, s50
	s_nop 0
	buffer_load_dwordx4 v141, s[8:11], s67 offen lds
	s_waitcnt vmcnt(8)
	s_waitcnt lgkmcnt(0)
	s_barrier
	s_setprio 1
	s_waitcnt lgkmcnt(7)
	v_mfma_f32_16x16x32_bf16 v[112:115], v[132:135], v[176:179], v[112:115]
	v_mfma_f32_16x16x32_bf16 v[116:119], v[152:155], v[176:179], v[116:119]
	s_waitcnt lgkmcnt(5)
	v_mfma_f32_16x16x32_bf16 v[96:99], v[132:135], v[184:187], v[96:99]
	v_mfma_f32_16x16x32_bf16 v[100:103], v[152:155], v[184:187], v[100:103]
	s_waitcnt lgkmcnt(3)
	v_mfma_f32_16x16x32_bf16 v[80:83], v[132:135], v[192:195], v[80:83]
	v_mfma_f32_16x16x32_bf16 v[84:87], v[152:155], v[192:195], v[84:87]
	s_waitcnt lgkmcnt(1)
	v_mfma_f32_16x16x32_bf16 v[64:67], v[132:135], v[200:203], v[64:67]
	v_mfma_f32_16x16x32_bf16 v[68:71], v[152:155], v[200:203], v[68:71]
	v_mfma_f32_16x16x32_bf16 v[112:115], v[148:151], v[180:183], v[112:115]
	v_mfma_f32_16x16x32_bf16 v[116:119], v[156:159], v[180:183], v[116:119]
	v_mfma_f32_16x16x32_bf16 v[96:99], v[148:151], v[188:191], v[96:99]
	v_mfma_f32_16x16x32_bf16 v[100:103], v[156:159], v[188:191], v[100:103]
	v_mfma_f32_16x16x32_bf16 v[80:83], v[148:151], v[196:199], v[80:83]
	v_mfma_f32_16x16x32_bf16 v[84:87], v[156:159], v[196:199], v[84:87]
	s_waitcnt lgkmcnt(0)
	v_mfma_f32_16x16x32_bf16 v[64:67], v[148:151], v[204:207], v[64:67]
	v_mfma_f32_16x16x32_bf16 v[68:71], v[156:159], v[204:207], v[68:71]
	s_setprio 0
	s_setprio 1
	v_mfma_f32_16x16x32_bf16 v[124:127], v[160:163], v[176:179], v[124:127]
	v_mfma_f32_16x16x32_bf16 v[120:123], v[168:171], v[176:179], v[120:123]
	v_mfma_f32_16x16x32_bf16 v[108:111], v[160:163], v[184:187], v[108:111]
	v_mfma_f32_16x16x32_bf16 v[104:107], v[168:171], v[184:187], v[104:107]
	v_mfma_f32_16x16x32_bf16 v[92:95], v[160:163], v[192:195], v[92:95]
	v_mfma_f32_16x16x32_bf16 v[88:91], v[168:171], v[192:195], v[88:91]
	v_mfma_f32_16x16x32_bf16 v[76:79], v[160:163], v[200:203], v[76:79]
	v_mfma_f32_16x16x32_bf16 v[72:75], v[168:171], v[200:203], v[72:75]
	v_mfma_f32_16x16x32_bf16 v[124:127], v[164:167], v[180:183], v[124:127]
	v_mfma_f32_16x16x32_bf16 v[120:123], v[172:175], v[180:183], v[120:123]
	v_mfma_f32_16x16x32_bf16 v[108:111], v[164:167], v[188:191], v[108:111]
	v_mfma_f32_16x16x32_bf16 v[104:107], v[172:175], v[188:191], v[104:107]
	v_mfma_f32_16x16x32_bf16 v[92:95], v[164:167], v[196:199], v[92:95]
	v_mfma_f32_16x16x32_bf16 v[88:91], v[172:175], v[196:199], v[88:91]
	v_mfma_f32_16x16x32_bf16 v[76:79], v[164:167], v[204:207], v[76:79]
	v_mfma_f32_16x16x32_bf16 v[72:75], v[172:175], v[204:207], v[72:75]
	s_setprio 0
	s_barrier
	s_mov_b32 m0, s52
	s_or_b32 s67, s65, 0x80
	ds_read_b128 v[176:179], v146 offset:49152
	ds_read_b128 v[180:183], v146 offset:50176
	ds_read_b128 v[184:187], v146 offset:51200
	ds_read_b128 v[188:191], v146 offset:52224
	ds_read_b128 v[192:195], v146 offset:53248
	ds_read_b128 v[196:199], v146 offset:54272
	ds_read_b128 v[200:203], v146 offset:55296
	ds_read_b128 v[204:207], v146 offset:56320
	buffer_load_dwordx4 v140, s[12:15], s67 offen lds
	s_mov_b32 m0, s33
	s_addk_i32 s65, 0x4080
	buffer_load_dwordx4 v142, s[12:15], s67 offen lds
	s_mov_b32 m0, s53
	s_addk_i32 s66, 0x80
	buffer_load_dwordx4 v140, s[12:15], s65 offen lds
	s_mov_b32 m0, s54
	s_nop 0
	buffer_load_dwordx4 v142, s[12:15], s65 offen lds
	s_mov_b32 m0, s46
	s_nop 0
	buffer_load_dwordx4 v139, s[8:11], s66 offen lds
	s_mov_b32 m0, s47
	s_nop 0
	buffer_load_dwordx4 v141, s[8:11], s66 offen lds
	s_waitcnt vmcnt(8)
	s_waitcnt lgkmcnt(0)
	s_barrier
	s_setprio 1
	s_waitcnt lgkmcnt(7)
	v_mfma_f32_16x16x32_bf16 v[48:51], v[132:135], v[176:179], v[48:51]
	v_mfma_f32_16x16x32_bf16 v[52:55], v[152:155], v[176:179], v[52:55]
	s_waitcnt lgkmcnt(5)
	v_mfma_f32_16x16x32_bf16 v[32:35], v[132:135], v[184:187], v[32:35]
	v_mfma_f32_16x16x32_bf16 v[36:39], v[152:155], v[184:187], v[36:39]
	s_waitcnt lgkmcnt(3)
	v_mfma_f32_16x16x32_bf16 v[16:19], v[132:135], v[192:195], v[16:19]
	v_mfma_f32_16x16x32_bf16 v[20:23], v[152:155], v[192:195], v[20:23]
	s_waitcnt lgkmcnt(1)
	v_mfma_f32_16x16x32_bf16 v[0:3], v[132:135], v[200:203], v[0:3]
	v_mfma_f32_16x16x32_bf16 v[4:7], v[152:155], v[200:203], v[4:7]
	v_mfma_f32_16x16x32_bf16 v[48:51], v[148:151], v[180:183], v[48:51]
	v_mfma_f32_16x16x32_bf16 v[52:55], v[156:159], v[180:183], v[52:55]
	v_mfma_f32_16x16x32_bf16 v[32:35], v[148:151], v[188:191], v[32:35]
	v_mfma_f32_16x16x32_bf16 v[36:39], v[156:159], v[188:191], v[36:39]
	v_mfma_f32_16x16x32_bf16 v[16:19], v[148:151], v[196:199], v[16:19]
	v_mfma_f32_16x16x32_bf16 v[20:23], v[156:159], v[196:199], v[20:23]
	s_waitcnt lgkmcnt(0)
	v_mfma_f32_16x16x32_bf16 v[0:3], v[148:151], v[204:207], v[0:3]
	v_mfma_f32_16x16x32_bf16 v[4:7], v[156:159], v[204:207], v[4:7]
	s_setprio 0
	s_setprio 1
	v_mfma_f32_16x16x32_bf16 v[60:63], v[160:163], v[176:179], v[60:63]
	v_mfma_f32_16x16x32_bf16 v[56:59], v[168:171], v[176:179], v[56:59]
	v_mfma_f32_16x16x32_bf16 v[44:47], v[160:163], v[184:187], v[44:47]
	v_mfma_f32_16x16x32_bf16 v[40:43], v[168:171], v[184:187], v[40:43]
	v_mfma_f32_16x16x32_bf16 v[28:31], v[160:163], v[192:195], v[28:31]
	v_mfma_f32_16x16x32_bf16 v[24:27], v[168:171], v[192:195], v[24:27]
	v_mfma_f32_16x16x32_bf16 v[12:15], v[160:163], v[200:203], v[12:15]
	v_mfma_f32_16x16x32_bf16 v[8:11], v[168:171], v[200:203], v[8:11]
	v_mfma_f32_16x16x32_bf16 v[60:63], v[164:167], v[180:183], v[60:63]
	v_mfma_f32_16x16x32_bf16 v[56:59], v[172:175], v[180:183], v[56:59]
	v_mfma_f32_16x16x32_bf16 v[44:47], v[164:167], v[188:191], v[44:47]
	v_mfma_f32_16x16x32_bf16 v[40:43], v[172:175], v[188:191], v[40:43]
	v_mfma_f32_16x16x32_bf16 v[28:31], v[164:167], v[196:199], v[28:31]
	v_mfma_f32_16x16x32_bf16 v[24:27], v[172:175], v[196:199], v[24:27]
	v_mfma_f32_16x16x32_bf16 v[12:15], v[164:167], v[204:207], v[12:15]
	v_mfma_f32_16x16x32_bf16 v[8:11], v[172:175], v[204:207], v[8:11]
	s_setprio 0
	s_add_i32 s63, s63, 2
	s_addk_i32 s64, 0x100
	s_cmp_gt_u32 s63, 13
	s_barrier
	s_cbranch_scc0 .LBB0_903
	s_and_b64 vcc, exec, s[30:31]
	s_cbranch_vccz .LBB0_906
	s_barrier

.LBB0_1000:
	v_add_u32_e32 v152, 0x10000, v141
	v_add_u32_e32 v168, 0x14000, v141
	ds_read_b128 v[132:135], v152
	ds_read_b128 v[144:147], v152 offset:1024
	ds_read_b128 v[148:151], v152 offset:2048
	ds_read_b128 v[152:155], v152 offset:3072
	ds_read_b128 v[156:159], v168
	ds_read_b128 v[160:163], v168 offset:1024
	ds_read_b128 v[164:167], v168 offset:2048
	ds_read_b128 v[168:171], v168 offset:3072
	s_add_i32 s75, s73, 0xfffc0080
	s_add_i32 s74, s75, s71
	s_cmp_eq_u32 s5, 12
	s_cselect_b64 s[76:77], -1, 0
	s_and_b64 s[14:15], s[76:77], exec
	s_cselect_b32 s74, s4, s74
	s_cselect_b32 s75, 0, s75
	s_add_i32 s14, s72, s73
	s_mov_b32 m0, s57
	ds_read_b128 v[172:175], v142
	ds_read_b128 v[176:179], v142 offset:1024
	ds_read_b128 v[180:183], v142 offset:2048
	ds_read_b128 v[184:187], v142 offset:3072
	ds_read_b128 v[188:191], v142 offset:4096
	ds_read_b128 v[192:195], v142 offset:5120
	ds_read_b128 v[196:199], v142 offset:6144
	ds_read_b128 v[200:203], v142 offset:7168
	buffer_load_dwordx4 v137, s[8:11], s14 offen lds
	s_mov_b32 m0, s59
	s_nop 0
	buffer_load_dwordx4 v139, s[8:11], s14 offen lds
	s_waitcnt vmcnt(8)
	s_waitcnt lgkmcnt(0)
	s_barrier
	s_setprio 1
	s_waitcnt lgkmcnt(7)
	v_mfma_f32_16x16x32_bf16 v[112:115], v[132:135], v[172:175], v[112:115]
	v_mfma_f32_16x16x32_bf16 v[116:119], v[148:151], v[172:175], v[116:119]
	s_waitcnt lgkmcnt(5)
	v_mfma_f32_16x16x32_bf16 v[96:99], v[132:135], v[180:183], v[96:99]
	v_mfma_f32_16x16x32_bf16 v[100:103], v[148:151], v[180:183], v[100:103]
	s_waitcnt lgkmcnt(3)
	v_mfma_f32_16x16x32_bf16 v[80:83], v[132:135], v[188:191], v[80:83]
	v_mfma_f32_16x16x32_bf16 v[84:87], v[148:151], v[188:191], v[84:87]
	s_waitcnt lgkmcnt(1)
	v_mfma_f32_16x16x32_bf16 v[68:71], v[132:135], v[196:199], v[68:71]
	v_mfma_f32_16x16x32_bf16 v[64:67], v[148:151], v[196:199], v[64:67]
	v_mfma_f32_16x16x32_bf16 v[112:115], v[144:147], v[176:179], v[112:115]
	v_mfma_f32_16x16x32_bf16 v[116:119], v[152:155], v[176:179], v[116:119]
	v_mfma_f32_16x16x32_bf16 v[96:99], v[144:147], v[184:187], v[96:99]
	v_mfma_f32_16x16x32_bf16 v[100:103], v[152:155], v[184:187], v[100:103]
	v_mfma_f32_16x16x32_bf16 v[80:83], v[144:147], v[192:195], v[80:83]
	v_mfma_f32_16x16x32_bf16 v[84:87], v[152:155], v[192:195], v[84:87]
	s_waitcnt lgkmcnt(0)
	v_mfma_f32_16x16x32_bf16 v[68:71], v[144:147], v[200:203], v[68:71]
	v_mfma_f32_16x16x32_bf16 v[64:67], v[152:155], v[200:203], v[64:67]
	s_setprio 0
	s_setprio 1
	v_mfma_f32_16x16x32_bf16 v[120:123], v[156:159], v[172:175], v[120:123]
	v_mfma_f32_16x16x32_bf16 v[124:127], v[164:167], v[172:175], v[124:127]
	v_mfma_f32_16x16x32_bf16 v[104:107], v[156:159], v[180:183], v[104:107]
	v_mfma_f32_16x16x32_bf16 v[108:111], v[164:167], v[180:183], v[108:111]
	v_mfma_f32_16x16x32_bf16 v[88:91], v[156:159], v[188:191], v[88:91]
	v_mfma_f32_16x16x32_bf16 v[92:95], v[164:167], v[188:191], v[92:95]
	v_mfma_f32_16x16x32_bf16 v[76:79], v[156:159], v[196:199], v[76:79]
	v_mfma_f32_16x16x32_bf16 v[72:75], v[164:167], v[196:199], v[72:75]
	v_mfma_f32_16x16x32_bf16 v[120:123], v[160:163], v[176:179], v[120:123]
	v_mfma_f32_16x16x32_bf16 v[124:127], v[168:171], v[176:179], v[124:127]
	v_mfma_f32_16x16x32_bf16 v[104:107], v[160:163], v[184:187], v[104:107]
	v_mfma_f32_16x16x32_bf16 v[108:111], v[168:171], v[184:187], v[108:111]
	v_mfma_f32_16x16x32_bf16 v[88:91], v[160:163], v[192:195], v[88:91]
	v_mfma_f32_16x16x32_bf16 v[92:95], v[168:171], v[192:195], v[92:95]
	v_mfma_f32_16x16x32_bf16 v[76:79], v[160:163], v[200:203], v[76:79]
	v_mfma_f32_16x16x32_bf16 v[72:75], v[168:171], v[200:203], v[72:75]
	s_setprio 0
	s_barrier
	s_mov_b32 m0, s7
	s_mov_b32 s14, s10
	s_mov_b32 s15, s11
	ds_read_b128 v[172:175], v142 offset:16384
	ds_read_b128 v[176:179], v142 offset:17408
	ds_read_b128 v[180:183], v142 offset:18432
	ds_read_b128 v[184:187], v142 offset:19456
	ds_read_b128 v[188:191], v142 offset:20480
	ds_read_b128 v[192:195], v142 offset:21504
	ds_read_b128 v[196:199], v142 offset:22528
	ds_read_b128 v[200:203], v142 offset:23552
	buffer_load_dwordx4 v138, s[12:15], s74 offen lds
	s_mov_b32 m0, s33
	s_add_i32 s78, s74, 0x4000
	s_and_b64 s[76:77], s[2:3], s[76:77]
	buffer_load_dwordx4 v140, s[12:15], s74 offen lds
	s_mov_b32 m0, s35
	s_and_b64 s[76:77], s[76:77], exec
	buffer_load_dwordx4 v138, s[12:15], s78 offen lds
	s_mov_b32 m0, s37
	s_cselect_b32 s76, s67, s72
	buffer_load_dwordx4 v140, s[12:15], s78 offen lds
	s_add_i32 s75, s75, s76
	s_mov_b32 m0, s1
	s_nop 0
	buffer_load_dwordx4 v137, s[8:11], s75 offen lds
	s_mov_b32 m0, s39
	s_nop 0
	buffer_load_dwordx4 v139, s[8:11], s75 offen lds
	s_waitcnt vmcnt(8)
	s_waitcnt lgkmcnt(0)
	s_barrier
	s_setprio 1
	s_waitcnt lgkmcnt(7)
	v_mfma_f32_16x16x32_bf16 v[48:51], v[132:135], v[172:175], v[48:51]
	v_mfma_f32_16x16x32_bf16 v[52:55], v[148:151], v[172:175], v[52:55]
	s_waitcnt lgkmcnt(5)
	v_mfma_f32_16x16x32_bf16 v[32:35], v[132:135], v[180:183], v[32:35]
	v_mfma_f32_16x16x32_bf16 v[36:39], v[148:151], v[180:183], v[36:39]
	s_waitcnt lgkmcnt(3)
	v_mfma_f32_16x16x32_bf16 v[16:19], v[132:135], v[188:191], v[16:19]
	v_mfma_f32_16x16x32_bf16 v[20:23], v[148:151], v[188:191], v[20:23]
	s_waitcnt lgkmcnt(1)
	v_mfma_f32_16x16x32_bf16 v[0:3], v[132:135], v[196:199], v[0:3]
	v_mfma_f32_16x16x32_bf16 v[4:7], v[148:151], v[196:199], v[4:7]
	v_mfma_f32_16x16x32_bf16 v[48:51], v[144:147], v[176:179], v[48:51]
	v_mfma_f32_16x16x32_bf16 v[52:55], v[152:155], v[176:179], v[52:55]
	v_mfma_f32_16x16x32_bf16 v[32:35], v[144:147], v[184:187], v[32:35]
	v_mfma_f32_16x16x32_bf16 v[36:39], v[152:155], v[184:187], v[36:39]
	v_mfma_f32_16x16x32_bf16 v[16:19], v[144:147], v[192:195], v[16:19]
	v_mfma_f32_16x16x32_bf16 v[20:23], v[152:155], v[192:195], v[20:23]
	s_waitcnt lgkmcnt(0)
	v_mfma_f32_16x16x32_bf16 v[0:3], v[144:147], v[200:203], v[0:3]
	v_mfma_f32_16x16x32_bf16 v[4:7], v[152:155], v[200:203], v[4:7]
	s_setprio 0
	s_setprio 1
	v_mfma_f32_16x16x32_bf16 v[60:63], v[156:159], v[172:175], v[60:63]
	v_mfma_f32_16x16x32_bf16 v[56:59], v[164:167], v[172:175], v[56:59]
	v_mfma_f32_16x16x32_bf16 v[44:47], v[156:159], v[180:183], v[44:47]
	v_mfma_f32_16x16x32_bf16 v[40:43], v[164:167], v[180:183], v[40:43]
	v_mfma_f32_16x16x32_bf16 v[28:31], v[156:159], v[188:191], v[28:31]
	v_mfma_f32_16x16x32_bf16 v[24:27], v[164:167], v[188:191], v[24:27]
	v_mfma_f32_16x16x32_bf16 v[12:15], v[156:159], v[196:199], v[12:15]
	v_mfma_f32_16x16x32_bf16 v[8:11], v[164:167], v[196:199], v[8:11]
	v_mfma_f32_16x16x32_bf16 v[60:63], v[160:163], v[176:179], v[60:63]
	v_mfma_f32_16x16x32_bf16 v[56:59], v[168:171], v[176:179], v[56:59]
	v_mfma_f32_16x16x32_bf16 v[44:47], v[160:163], v[184:187], v[44:47]
	v_mfma_f32_16x16x32_bf16 v[40:43], v[168:171], v[184:187], v[40:43]
	v_mfma_f32_16x16x32_bf16 v[28:31], v[160:163], v[192:195], v[28:31]
	v_mfma_f32_16x16x32_bf16 v[24:27], v[168:171], v[192:195], v[24:27]
	v_mfma_f32_16x16x32_bf16 v[12:15], v[160:163], v[200:203], v[12:15]
	v_mfma_f32_16x16x32_bf16 v[8:11], v[168:171], v[200:203], v[8:11]
	s_setprio 0
	s_barrier
	v_add_u32_e32 v152, 0x18000, v141
	v_add_u32_e32 v168, 0x1c000, v141
	ds_read_b128 v[132:135], v152
	ds_read_b128 v[144:147], v152 offset:1024
	ds_read_b128 v[148:151], v152 offset:2048
	ds_read_b128 v[152:155], v152 offset:3072
	ds_read_b128 v[156:159], v168
	ds_read_b128 v[160:163], v168 offset:1024
	ds_read_b128 v[164:167], v168 offset:2048
	ds_read_b128 v[168:171], v168 offset:3072
	s_add_i32 s76, s75, 0x40000
	s_mov_b32 m0, s40
	ds_read_b128 v[172:175], v142 offset:32768
	ds_read_b128 v[176:179], v142 offset:33792
	ds_read_b128 v[180:183], v142 offset:34816
	ds_read_b128 v[184:187], v142 offset:35840
	ds_read_b128 v[188:191], v142 offset:36864
	ds_read_b128 v[192:195], v142 offset:37888
	ds_read_b128 v[196:199], v142 offset:38912
	ds_read_b128 v[200:203], v142 offset:39936
	buffer_load_dwordx4 v137, s[8:11], s76 offen lds
	s_mov_b32 m0, s41
	s_nop 0
	buffer_load_dwordx4 v139, s[8:11], s76 offen lds
	s_waitcnt vmcnt(8)
	s_waitcnt lgkmcnt(0)
	s_barrier
	s_setprio 1
	s_waitcnt lgkmcnt(7)
	v_mfma_f32_16x16x32_bf16 v[112:115], v[132:135], v[172:175], v[112:115]
	v_mfma_f32_16x16x32_bf16 v[116:119], v[148:151], v[172:175], v[116:119]
	s_waitcnt lgkmcnt(5)
	v_mfma_f32_16x16x32_bf16 v[96:99], v[132:135], v[180:183], v[96:99]
	v_mfma_f32_16x16x32_bf16 v[100:103], v[148:151], v[180:183], v[100:103]
	s_waitcnt lgkmcnt(3)
	v_mfma_f32_16x16x32_bf16 v[80:83], v[132:135], v[188:191], v[80:83]
	v_mfma_f32_16x16x32_bf16 v[84:87], v[148:151], v[188:191], v[84:87]
	s_waitcnt lgkmcnt(1)
	v_mfma_f32_16x16x32_bf16 v[68:71], v[132:135], v[196:199], v[68:71]
	v_mfma_f32_16x16x32_bf16 v[64:67], v[148:151], v[196:199], v[64:67]
	v_mfma_f32_16x16x32_bf16 v[112:115], v[144:147], v[176:179], v[112:115]
	v_mfma_f32_16x16x32_bf16 v[116:119], v[152:155], v[176:179], v[116:119]
	v_mfma_f32_16x16x32_bf16 v[96:99], v[144:147], v[184:187], v[96:99]
	v_mfma_f32_16x16x32_bf16 v[100:103], v[152:155], v[184:187], v[100:103]
	v_mfma_f32_16x16x32_bf16 v[80:83], v[144:147], v[192:195], v[80:83]
	v_mfma_f32_16x16x32_bf16 v[84:87], v[152:155], v[192:195], v[84:87]
	s_waitcnt lgkmcnt(0)
	v_mfma_f32_16x16x32_bf16 v[68:71], v[144:147], v[200:203], v[68:71]
	v_mfma_f32_16x16x32_bf16 v[64:67], v[152:155], v[200:203], v[64:67]
	s_setprio 0
	s_setprio 1
	v_mfma_f32_16x16x32_bf16 v[120:123], v[156:159], v[172:175], v[120:123]
	v_mfma_f32_16x16x32_bf16 v[124:127], v[164:167], v[172:175], v[124:127]
	v_mfma_f32_16x16x32_bf16 v[104:107], v[156:159], v[180:183], v[104:107]
	v_mfma_f32_16x16x32_bf16 v[108:111], v[164:167], v[180:183], v[108:111]
	v_mfma_f32_16x16x32_bf16 v[88:91], v[156:159], v[188:191], v[88:91]
	v_mfma_f32_16x16x32_bf16 v[92:95], v[164:167], v[188:191], v[92:95]
	v_mfma_f32_16x16x32_bf16 v[76:79], v[156:159], v[196:199], v[76:79]
	v_mfma_f32_16x16x32_bf16 v[72:75], v[164:167], v[196:199], v[72:75]
	v_mfma_f32_16x16x32_bf16 v[120:123], v[160:163], v[176:179], v[120:123]
	v_mfma_f32_16x16x32_bf16 v[124:127], v[168:171], v[176:179], v[124:127]
	v_mfma_f32_16x16x32_bf16 v[104:107], v[160:163], v[184:187], v[104:107]
	v_mfma_f32_16x16x32_bf16 v[108:111], v[168:171], v[184:187], v[108:111]
	v_mfma_f32_16x16x32_bf16 v[88:91], v[160:163], v[192:195], v[88:91]
	v_mfma_f32_16x16x32_bf16 v[92:95], v[168:171], v[192:195], v[92:95]
	v_mfma_f32_16x16x32_bf16 v[76:79], v[160:163], v[200:203], v[76:79]
	v_mfma_f32_16x16x32_bf16 v[72:75], v[168:171], v[200:203], v[72:75]
	s_setprio 0
	s_barrier
	s_mov_b32 m0, s44
	s_or_b32 s76, s74, 0x80
	ds_read_b128 v[172:175], v142 offset:49152
	ds_read_b128 v[176:179], v142 offset:50176
	ds_read_b128 v[180:183], v142 offset:51200
	ds_read_b128 v[184:187], v142 offset:52224
	ds_read_b128 v[188:191], v142 offset:53248
	ds_read_b128 v[192:195], v142 offset:54272
	ds_read_b128 v[196:199], v142 offset:55296
	ds_read_b128 v[200:203], v142 offset:56320
	buffer_load_dwordx4 v138, s[12:15], s76 offen lds
	s_mov_b32 m0, s45
	s_addk_i32 s74, 0x4080
	buffer_load_dwordx4 v140, s[12:15], s76 offen lds
	s_mov_b32 m0, s54
	s_addk_i32 s75, 0x80
	buffer_load_dwordx4 v138, s[12:15], s74 offen lds
	s_mov_b32 m0, s55
	s_nop 0
	buffer_load_dwordx4 v140, s[12:15], s74 offen lds
	s_mov_b32 m0, s46
	s_nop 0
	buffer_load_dwordx4 v137, s[8:11], s75 offen lds
	s_mov_b32 m0, s47
	s_nop 0
	buffer_load_dwordx4 v139, s[8:11], s75 offen lds
	s_waitcnt vmcnt(8)
	s_waitcnt lgkmcnt(0)
	s_barrier
	s_setprio 1
	s_waitcnt lgkmcnt(7)
	v_mfma_f32_16x16x32_bf16 v[48:51], v[132:135], v[172:175], v[48:51]
	v_mfma_f32_16x16x32_bf16 v[52:55], v[148:151], v[172:175], v[52:55]
	s_waitcnt lgkmcnt(5)
	v_mfma_f32_16x16x32_bf16 v[32:35], v[132:135], v[180:183], v[32:35]
	v_mfma_f32_16x16x32_bf16 v[36:39], v[148:151], v[180:183], v[36:39]
	s_waitcnt lgkmcnt(3)
	v_mfma_f32_16x16x32_bf16 v[16:19], v[132:135], v[188:191], v[16:19]
	v_mfma_f32_16x16x32_bf16 v[20:23], v[148:151], v[188:191], v[20:23]
	s_waitcnt lgkmcnt(1)
	v_mfma_f32_16x16x32_bf16 v[0:3], v[132:135], v[196:199], v[0:3]
	v_mfma_f32_16x16x32_bf16 v[4:7], v[148:151], v[196:199], v[4:7]
	v_mfma_f32_16x16x32_bf16 v[48:51], v[144:147], v[176:179], v[48:51]
	v_mfma_f32_16x16x32_bf16 v[52:55], v[152:155], v[176:179], v[52:55]
	v_mfma_f32_16x16x32_bf16 v[32:35], v[144:147], v[184:187], v[32:35]
	v_mfma_f32_16x16x32_bf16 v[36:39], v[152:155], v[184:187], v[36:39]
	v_mfma_f32_16x16x32_bf16 v[16:19], v[144:147], v[192:195], v[16:19]
	v_mfma_f32_16x16x32_bf16 v[20:23], v[152:155], v[192:195], v[20:23]
	s_waitcnt lgkmcnt(0)
	v_mfma_f32_16x16x32_bf16 v[0:3], v[144:147], v[200:203], v[0:3]
	v_mfma_f32_16x16x32_bf16 v[4:7], v[152:155], v[200:203], v[4:7]
	s_setprio 0
	s_setprio 1
	v_mfma_f32_16x16x32_bf16 v[60:63], v[156:159], v[172:175], v[60:63]
	v_mfma_f32_16x16x32_bf16 v[56:59], v[164:167], v[172:175], v[56:59]
	v_mfma_f32_16x16x32_bf16 v[44:47], v[156:159], v[180:183], v[44:47]
	v_mfma_f32_16x16x32_bf16 v[40:43], v[164:167], v[180:183], v[40:43]
	v_mfma_f32_16x16x32_bf16 v[28:31], v[156:159], v[188:191], v[28:31]
	v_mfma_f32_16x16x32_bf16 v[24:27], v[164:167], v[188:191], v[24:27]
	v_mfma_f32_16x16x32_bf16 v[12:15], v[156:159], v[196:199], v[12:15]
	v_mfma_f32_16x16x32_bf16 v[8:11], v[164:167], v[196:199], v[8:11]
	v_mfma_f32_16x16x32_bf16 v[60:63], v[160:163], v[176:179], v[60:63]
	v_mfma_f32_16x16x32_bf16 v[56:59], v[168:171], v[176:179], v[56:59]
	v_mfma_f32_16x16x32_bf16 v[44:47], v[160:163], v[184:187], v[44:47]
	v_mfma_f32_16x16x32_bf16 v[40:43], v[168:171], v[184:187], v[40:43]
	v_mfma_f32_16x16x32_bf16 v[28:31], v[160:163], v[192:195], v[28:31]
	v_mfma_f32_16x16x32_bf16 v[24:27], v[168:171], v[192:195], v[24:27]
	v_mfma_f32_16x16x32_bf16 v[12:15], v[160:163], v[200:203], v[12:15]
	v_mfma_f32_16x16x32_bf16 v[8:11], v[168:171], v[200:203], v[8:11]
	s_setprio 0
	s_add_i32 s5, s5, 2
	s_addk_i32 s73, 0x100
	s_cmp_gt_u32 s5, 13
	s_barrier
	s_cbranch_scc0 .LBB0_1000
	s_and_b64 vcc, exec, s[30:31]
	s_cbranch_vccz .LBB0_1003
	s_barrier

.LBB0_1148:
	v_add_u32_e32 v145, 0x10000, v143
	ds_read_b128 v[132:135], v145
	ds_read_b128 v[146:149], v145 offset:1024
	ds_read_b128 v[150:153], v145 offset:2048
	ds_read_b128 v[154:157], v145 offset:3072
	v_add_u32_e32 v145, 0x14000, v143
	ds_read_b128 v[158:161], v145
	ds_read_b128 v[162:165], v145 offset:1024
	ds_read_b128 v[166:169], v145 offset:2048
	ds_read_b128 v[170:173], v145 offset:3072
	s_add_i32 s64, s60, 0xfffc0080
	s_add_i32 s61, s64, s56
	s_cmp_eq_u32 s59, 12
	s_cselect_b64 s[62:63], -1, 0
	s_and_b64 s[14:15], s[62:63], exec
	s_cselect_b32 s61, s58, s61
	s_cselect_b32 s64, 0, s64
	s_add_i32 s14, s57, s60
	s_mov_b32 m0, s49
	ds_read_b128 v[174:177], v144
	ds_read_b128 v[178:181], v144 offset:1024
	ds_read_b128 v[182:185], v144 offset:2048
	ds_read_b128 v[186:189], v144 offset:3072
	ds_read_b128 v[190:193], v144 offset:4096
	ds_read_b128 v[194:197], v144 offset:5120
	ds_read_b128 v[198:201], v144 offset:6144
	ds_read_b128 v[202:205], v144 offset:7168
	buffer_load_dwordx4 v137, s[8:11], s14 offen lds
	s_mov_b32 m0, s0
	s_nop 0
	buffer_load_dwordx4 v139, s[8:11], s14 offen lds
	s_waitcnt vmcnt(8)
	s_waitcnt lgkmcnt(0)
	s_barrier
	s_setprio 1
	s_waitcnt lgkmcnt(7)
	v_mfma_f32_16x16x32_bf16 v[112:115], v[132:135], v[174:177], v[112:115]
	v_mfma_f32_16x16x32_bf16 v[116:119], v[150:153], v[174:177], v[116:119]
	s_waitcnt lgkmcnt(5)
	v_mfma_f32_16x16x32_bf16 v[96:99], v[132:135], v[182:185], v[96:99]
	v_mfma_f32_16x16x32_bf16 v[100:103], v[150:153], v[182:185], v[100:103]
	s_waitcnt lgkmcnt(3)
	v_mfma_f32_16x16x32_bf16 v[80:83], v[132:135], v[190:193], v[80:83]
	v_mfma_f32_16x16x32_bf16 v[84:87], v[150:153], v[190:193], v[84:87]
	s_waitcnt lgkmcnt(1)
	v_mfma_f32_16x16x32_bf16 v[64:67], v[132:135], v[198:201], v[64:67]
	v_mfma_f32_16x16x32_bf16 v[68:71], v[150:153], v[198:201], v[68:71]
	v_mfma_f32_16x16x32_bf16 v[112:115], v[146:149], v[178:181], v[112:115]
	v_mfma_f32_16x16x32_bf16 v[116:119], v[154:157], v[178:181], v[116:119]
	v_mfma_f32_16x16x32_bf16 v[96:99], v[146:149], v[186:189], v[96:99]
	v_mfma_f32_16x16x32_bf16 v[100:103], v[154:157], v[186:189], v[100:103]
	v_mfma_f32_16x16x32_bf16 v[80:83], v[146:149], v[194:197], v[80:83]
	v_mfma_f32_16x16x32_bf16 v[84:87], v[154:157], v[194:197], v[84:87]
	s_waitcnt lgkmcnt(0)
	v_mfma_f32_16x16x32_bf16 v[64:67], v[146:149], v[202:205], v[64:67]
	v_mfma_f32_16x16x32_bf16 v[68:71], v[154:157], v[202:205], v[68:71]
	s_setprio 0
	s_setprio 1
	v_mfma_f32_16x16x32_bf16 v[124:127], v[158:161], v[174:177], v[124:127]
	v_mfma_f32_16x16x32_bf16 v[120:123], v[166:169], v[174:177], v[120:123]
	v_mfma_f32_16x16x32_bf16 v[108:111], v[158:161], v[182:185], v[108:111]
	v_mfma_f32_16x16x32_bf16 v[104:107], v[166:169], v[182:185], v[104:107]
	v_mfma_f32_16x16x32_bf16 v[92:95], v[158:161], v[190:193], v[92:95]
	v_mfma_f32_16x16x32_bf16 v[88:91], v[166:169], v[190:193], v[88:91]
	v_mfma_f32_16x16x32_bf16 v[76:79], v[158:161], v[198:201], v[76:79]
	v_mfma_f32_16x16x32_bf16 v[72:75], v[166:169], v[198:201], v[72:75]
	v_mfma_f32_16x16x32_bf16 v[124:127], v[162:165], v[178:181], v[124:127]
	v_mfma_f32_16x16x32_bf16 v[120:123], v[170:173], v[178:181], v[120:123]
	v_mfma_f32_16x16x32_bf16 v[108:111], v[162:165], v[186:189], v[108:111]
	v_mfma_f32_16x16x32_bf16 v[104:107], v[170:173], v[186:189], v[104:107]
	v_mfma_f32_16x16x32_bf16 v[92:95], v[162:165], v[194:197], v[92:95]
	v_mfma_f32_16x16x32_bf16 v[88:91], v[170:173], v[194:197], v[88:91]
	v_mfma_f32_16x16x32_bf16 v[76:79], v[162:165], v[202:205], v[76:79]
	v_mfma_f32_16x16x32_bf16 v[72:75], v[170:173], v[202:205], v[72:75]
	s_setprio 0
	s_barrier
	s_mov_b32 m0, s28
	s_mov_b32 s14, s10
	s_mov_b32 s15, s11
	ds_read_b128 v[174:177], v144 offset:16384
	ds_read_b128 v[178:181], v144 offset:17408
	ds_read_b128 v[182:185], v144 offset:18432
	ds_read_b128 v[186:189], v144 offset:19456
	ds_read_b128 v[190:193], v144 offset:20480
	ds_read_b128 v[194:197], v144 offset:21504
	ds_read_b128 v[198:201], v144 offset:22528
	ds_read_b128 v[202:205], v144 offset:23552
	buffer_load_dwordx4 v138, s[12:15], s61 offen lds
	s_mov_b32 m0, s29
	s_add_i32 s65, s61, 0x4000
	s_and_b64 s[62:63], s[2:3], s[62:63]
	buffer_load_dwordx4 v140, s[12:15], s61 offen lds
	s_mov_b32 m0, s30
	s_and_b64 s[62:63], s[62:63], exec
	buffer_load_dwordx4 v138, s[12:15], s65 offen lds
	s_mov_b32 m0, s31
	s_cselect_b32 s62, s52, s57
	buffer_load_dwordx4 v140, s[12:15], s65 offen lds
	s_add_i32 s62, s64, s62
	s_mov_b32 m0, s7
	s_nop 0
	buffer_load_dwordx4 v137, s[8:11], s62 offen lds
	s_mov_b32 m0, s33
	s_nop 0
	buffer_load_dwordx4 v139, s[8:11], s62 offen lds
	s_waitcnt vmcnt(8)
	s_waitcnt lgkmcnt(0)
	s_barrier
	s_setprio 1
	s_waitcnt lgkmcnt(7)
	v_mfma_f32_16x16x32_bf16 v[48:51], v[132:135], v[174:177], v[48:51]
	v_mfma_f32_16x16x32_bf16 v[52:55], v[150:153], v[174:177], v[52:55]
	s_waitcnt lgkmcnt(5)
	v_mfma_f32_16x16x32_bf16 v[32:35], v[132:135], v[182:185], v[32:35]
	v_mfma_f32_16x16x32_bf16 v[36:39], v[150:153], v[182:185], v[36:39]
	s_waitcnt lgkmcnt(3)
	v_mfma_f32_16x16x32_bf16 v[16:19], v[132:135], v[190:193], v[16:19]
	v_mfma_f32_16x16x32_bf16 v[20:23], v[150:153], v[190:193], v[20:23]
	s_waitcnt lgkmcnt(1)
	v_mfma_f32_16x16x32_bf16 v[0:3], v[132:135], v[198:201], v[0:3]
	v_mfma_f32_16x16x32_bf16 v[4:7], v[150:153], v[198:201], v[4:7]
	v_mfma_f32_16x16x32_bf16 v[48:51], v[146:149], v[178:181], v[48:51]
	v_mfma_f32_16x16x32_bf16 v[52:55], v[154:157], v[178:181], v[52:55]
	v_mfma_f32_16x16x32_bf16 v[32:35], v[146:149], v[186:189], v[32:35]
	v_mfma_f32_16x16x32_bf16 v[36:39], v[154:157], v[186:189], v[36:39]
	v_mfma_f32_16x16x32_bf16 v[16:19], v[146:149], v[194:197], v[16:19]
	v_mfma_f32_16x16x32_bf16 v[20:23], v[154:157], v[194:197], v[20:23]
	s_waitcnt lgkmcnt(0)
	v_mfma_f32_16x16x32_bf16 v[0:3], v[146:149], v[202:205], v[0:3]
	v_mfma_f32_16x16x32_bf16 v[4:7], v[154:157], v[202:205], v[4:7]
	s_setprio 0
	s_setprio 1
	v_mfma_f32_16x16x32_bf16 v[60:63], v[158:161], v[174:177], v[60:63]
	v_mfma_f32_16x16x32_bf16 v[56:59], v[166:169], v[174:177], v[56:59]
	v_mfma_f32_16x16x32_bf16 v[44:47], v[158:161], v[182:185], v[44:47]
	v_mfma_f32_16x16x32_bf16 v[40:43], v[166:169], v[182:185], v[40:43]
	v_mfma_f32_16x16x32_bf16 v[28:31], v[158:161], v[190:193], v[28:31]
	v_mfma_f32_16x16x32_bf16 v[24:27], v[166:169], v[190:193], v[24:27]
	v_mfma_f32_16x16x32_bf16 v[12:15], v[158:161], v[198:201], v[12:15]
	v_mfma_f32_16x16x32_bf16 v[8:11], v[166:169], v[198:201], v[8:11]
	v_mfma_f32_16x16x32_bf16 v[60:63], v[162:165], v[178:181], v[60:63]
	v_mfma_f32_16x16x32_bf16 v[56:59], v[170:173], v[178:181], v[56:59]
	v_mfma_f32_16x16x32_bf16 v[44:47], v[162:165], v[186:189], v[44:47]
	v_mfma_f32_16x16x32_bf16 v[40:43], v[170:173], v[186:189], v[40:43]
	v_mfma_f32_16x16x32_bf16 v[28:31], v[162:165], v[194:197], v[28:31]
	v_mfma_f32_16x16x32_bf16 v[24:27], v[170:173], v[194:197], v[24:27]
	v_mfma_f32_16x16x32_bf16 v[12:15], v[162:165], v[202:205], v[12:15]
	v_mfma_f32_16x16x32_bf16 v[8:11], v[170:173], v[202:205], v[8:11]
	s_setprio 0
	s_barrier
	v_add_u32_e32 v145, 0x18000, v143
	ds_read_b128 v[132:135], v145
	ds_read_b128 v[146:149], v145 offset:1024
	ds_read_b128 v[150:153], v145 offset:2048
	ds_read_b128 v[154:157], v145 offset:3072
	v_add_u32_e32 v145, 0x1c000, v143
	ds_read_b128 v[158:161], v145
	ds_read_b128 v[162:165], v145 offset:1024
	ds_read_b128 v[166:169], v145 offset:2048
	ds_read_b128 v[170:173], v145 offset:3072
	s_add_i32 s63, s62, 0x40000
	s_mov_b32 m0, s35
	ds_read_b128 v[174:177], v144 offset:32768
	ds_read_b128 v[178:181], v144 offset:33792
	ds_read_b128 v[182:185], v144 offset:34816
	ds_read_b128 v[186:189], v144 offset:35840
	ds_read_b128 v[190:193], v144 offset:36864
	ds_read_b128 v[194:197], v144 offset:37888
	ds_read_b128 v[198:201], v144 offset:38912
	ds_read_b128 v[202:205], v144 offset:39936
	buffer_load_dwordx4 v137, s[8:11], s63 offen lds
	s_mov_b32 m0, s37
	s_nop 0
	buffer_load_dwordx4 v139, s[8:11], s63 offen lds
	s_waitcnt vmcnt(8)
	s_waitcnt lgkmcnt(0)
	s_barrier
	s_setprio 1
	s_waitcnt lgkmcnt(7)
	v_mfma_f32_16x16x32_bf16 v[112:115], v[132:135], v[174:177], v[112:115]
	v_mfma_f32_16x16x32_bf16 v[116:119], v[150:153], v[174:177], v[116:119]
	s_waitcnt lgkmcnt(5)
	v_mfma_f32_16x16x32_bf16 v[96:99], v[132:135], v[182:185], v[96:99]
	v_mfma_f32_16x16x32_bf16 v[100:103], v[150:153], v[182:185], v[100:103]
	s_waitcnt lgkmcnt(3)
	v_mfma_f32_16x16x32_bf16 v[80:83], v[132:135], v[190:193], v[80:83]
	v_mfma_f32_16x16x32_bf16 v[84:87], v[150:153], v[190:193], v[84:87]
	s_waitcnt lgkmcnt(1)
	v_mfma_f32_16x16x32_bf16 v[64:67], v[132:135], v[198:201], v[64:67]
	v_mfma_f32_16x16x32_bf16 v[68:71], v[150:153], v[198:201], v[68:71]
	v_mfma_f32_16x16x32_bf16 v[112:115], v[146:149], v[178:181], v[112:115]
	v_mfma_f32_16x16x32_bf16 v[116:119], v[154:157], v[178:181], v[116:119]
	v_mfma_f32_16x16x32_bf16 v[96:99], v[146:149], v[186:189], v[96:99]
	v_mfma_f32_16x16x32_bf16 v[100:103], v[154:157], v[186:189], v[100:103]
	v_mfma_f32_16x16x32_bf16 v[80:83], v[146:149], v[194:197], v[80:83]
	v_mfma_f32_16x16x32_bf16 v[84:87], v[154:157], v[194:197], v[84:87]
	s_waitcnt lgkmcnt(0)
	v_mfma_f32_16x16x32_bf16 v[64:67], v[146:149], v[202:205], v[64:67]
	v_mfma_f32_16x16x32_bf16 v[68:71], v[154:157], v[202:205], v[68:71]
	s_setprio 0
	s_setprio 1
	v_mfma_f32_16x16x32_bf16 v[124:127], v[158:161], v[174:177], v[124:127]
	v_mfma_f32_16x16x32_bf16 v[120:123], v[166:169], v[174:177], v[120:123]
	v_mfma_f32_16x16x32_bf16 v[108:111], v[158:161], v[182:185], v[108:111]
	v_mfma_f32_16x16x32_bf16 v[104:107], v[166:169], v[182:185], v[104:107]
	v_mfma_f32_16x16x32_bf16 v[92:95], v[158:161], v[190:193], v[92:95]
	v_mfma_f32_16x16x32_bf16 v[88:91], v[166:169], v[190:193], v[88:91]
	v_mfma_f32_16x16x32_bf16 v[76:79], v[158:161], v[198:201], v[76:79]
	v_mfma_f32_16x16x32_bf16 v[72:75], v[166:169], v[198:201], v[72:75]
	v_mfma_f32_16x16x32_bf16 v[124:127], v[162:165], v[178:181], v[124:127]
	v_mfma_f32_16x16x32_bf16 v[120:123], v[170:173], v[178:181], v[120:123]
	v_mfma_f32_16x16x32_bf16 v[108:111], v[162:165], v[186:189], v[108:111]
	v_mfma_f32_16x16x32_bf16 v[104:107], v[170:173], v[186:189], v[104:107]
	v_mfma_f32_16x16x32_bf16 v[92:95], v[162:165], v[194:197], v[92:95]
	v_mfma_f32_16x16x32_bf16 v[88:91], v[170:173], v[194:197], v[88:91]
	v_mfma_f32_16x16x32_bf16 v[76:79], v[162:165], v[202:205], v[76:79]
	v_mfma_f32_16x16x32_bf16 v[72:75], v[170:173], v[202:205], v[72:75]
	s_setprio 0
	s_barrier
	s_mov_b32 m0, s40
	s_or_b32 s63, s61, 0x80
	ds_read_b128 v[174:177], v144 offset:49152
	ds_read_b128 v[178:181], v144 offset:50176
	ds_read_b128 v[182:185], v144 offset:51200
	ds_read_b128 v[186:189], v144 offset:52224
	ds_read_b128 v[190:193], v144 offset:53248
	ds_read_b128 v[194:197], v144 offset:54272
	ds_read_b128 v[198:201], v144 offset:55296
	ds_read_b128 v[202:205], v144 offset:56320
	buffer_load_dwordx4 v138, s[12:15], s63 offen lds
	s_mov_b32 m0, s41
	s_addk_i32 s61, 0x4080
	buffer_load_dwordx4 v140, s[12:15], s63 offen lds
	s_mov_b32 m0, s46
	s_addk_i32 s62, 0x80
	buffer_load_dwordx4 v138, s[12:15], s61 offen lds
	s_mov_b32 m0, s47
	s_nop 0
	buffer_load_dwordx4 v140, s[12:15], s61 offen lds
	s_mov_b32 m0, s44
	s_nop 0
	buffer_load_dwordx4 v137, s[8:11], s62 offen lds
	s_mov_b32 m0, s45
	s_nop 0
	buffer_load_dwordx4 v139, s[8:11], s62 offen lds
	s_waitcnt vmcnt(8)
	s_waitcnt lgkmcnt(0)
	s_barrier
	s_setprio 1
	s_waitcnt lgkmcnt(7)
	v_mfma_f32_16x16x32_bf16 v[48:51], v[132:135], v[174:177], v[48:51]
	v_mfma_f32_16x16x32_bf16 v[52:55], v[150:153], v[174:177], v[52:55]
	s_waitcnt lgkmcnt(5)
	v_mfma_f32_16x16x32_bf16 v[32:35], v[132:135], v[182:185], v[32:35]
	v_mfma_f32_16x16x32_bf16 v[36:39], v[150:153], v[182:185], v[36:39]
	s_waitcnt lgkmcnt(3)
	v_mfma_f32_16x16x32_bf16 v[16:19], v[132:135], v[190:193], v[16:19]
	v_mfma_f32_16x16x32_bf16 v[20:23], v[150:153], v[190:193], v[20:23]
	s_waitcnt lgkmcnt(1)
	v_mfma_f32_16x16x32_bf16 v[0:3], v[132:135], v[198:201], v[0:3]
	v_mfma_f32_16x16x32_bf16 v[4:7], v[150:153], v[198:201], v[4:7]
	v_mfma_f32_16x16x32_bf16 v[48:51], v[146:149], v[178:181], v[48:51]
	v_mfma_f32_16x16x32_bf16 v[52:55], v[154:157], v[178:181], v[52:55]
	v_mfma_f32_16x16x32_bf16 v[32:35], v[146:149], v[186:189], v[32:35]
	v_mfma_f32_16x16x32_bf16 v[36:39], v[154:157], v[186:189], v[36:39]
	v_mfma_f32_16x16x32_bf16 v[16:19], v[146:149], v[194:197], v[16:19]
	v_mfma_f32_16x16x32_bf16 v[20:23], v[154:157], v[194:197], v[20:23]
	s_waitcnt lgkmcnt(0)
	v_mfma_f32_16x16x32_bf16 v[0:3], v[146:149], v[202:205], v[0:3]
	v_mfma_f32_16x16x32_bf16 v[4:7], v[154:157], v[202:205], v[4:7]
	s_setprio 0
	s_setprio 1
	v_mfma_f32_16x16x32_bf16 v[60:63], v[158:161], v[174:177], v[60:63]
	v_mfma_f32_16x16x32_bf16 v[56:59], v[166:169], v[174:177], v[56:59]
	v_mfma_f32_16x16x32_bf16 v[44:47], v[158:161], v[182:185], v[44:47]
	v_mfma_f32_16x16x32_bf16 v[40:43], v[166:169], v[182:185], v[40:43]
	v_mfma_f32_16x16x32_bf16 v[28:31], v[158:161], v[190:193], v[28:31]
	v_mfma_f32_16x16x32_bf16 v[24:27], v[166:169], v[190:193], v[24:27]
	v_mfma_f32_16x16x32_bf16 v[12:15], v[158:161], v[198:201], v[12:15]
	v_mfma_f32_16x16x32_bf16 v[8:11], v[166:169], v[198:201], v[8:11]
	v_mfma_f32_16x16x32_bf16 v[60:63], v[162:165], v[178:181], v[60:63]
	v_mfma_f32_16x16x32_bf16 v[56:59], v[170:173], v[178:181], v[56:59]
	v_mfma_f32_16x16x32_bf16 v[44:47], v[162:165], v[186:189], v[44:47]
	v_mfma_f32_16x16x32_bf16 v[40:43], v[170:173], v[186:189], v[40:43]
	v_mfma_f32_16x16x32_bf16 v[28:31], v[162:165], v[194:197], v[28:31]
	v_mfma_f32_16x16x32_bf16 v[24:27], v[170:173], v[194:197], v[24:27]
	v_mfma_f32_16x16x32_bf16 v[12:15], v[162:165], v[202:205], v[12:15]
	v_mfma_f32_16x16x32_bf16 v[8:11], v[170:173], v[202:205], v[8:11]
	s_setprio 0
	s_add_i32 s59, s59, 2
	s_addk_i32 s60, 0x100
	s_cmp_gt_u32 s59, 13
	s_barrier
	s_cbranch_scc0 .LBB0_1148
	s_and_b64 vcc, exec, s[26:27]
	s_cbranch_vccz .LBB0_1151
	s_barrier

.LBB0_1560:
	v_add_u32_e32 v1, 0x10000, v154
	ds_read_b128 v[132:135], v1
	ds_read_b128 v[136:139], v1 offset:1024
	ds_read_b128 v[140:143], v1 offset:2048
	ds_read_b128 v[144:147], v1 offset:3072
	v_add_u32_e32 v1, 0x14000, v154
	ds_read_b128 v[156:159], v1
	ds_read_b128 v[160:163], v1 offset:1024
	ds_read_b128 v[164:167], v1 offset:2048
	ds_read_b128 v[168:171], v1 offset:3072
	s_add_i32 s77, s75, 0xfffe0080
	s_add_i32 s76, s77, s70
	s_cmp_eq_u32 s74, 4
	s_cselect_b64 s[54:55], -1, 0
	s_and_b64 s[14:15], s[54:55], exec
	s_cselect_b32 s76, s73, s76
	s_cselect_b32 s77, 0, s77
	s_add_i32 s14, s71, s75
	s_mov_b32 m0, s59
	ds_read_b128 v[172:175], v155
	ds_read_b128 v[176:179], v155 offset:1024
	ds_read_b128 v[180:183], v155 offset:2048
	ds_read_b128 v[184:187], v155 offset:3072
	ds_read_b128 v[188:191], v155 offset:4096
	ds_read_b128 v[192:195], v155 offset:5120
	ds_read_b128 v[200:203], v155 offset:6144
	ds_read_b128 v[204:207], v155 offset:7168
	buffer_load_dwordx4 v149, s[8:11], s14 offen lds
	s_mov_b32 m0, s61
	s_nop 0
	buffer_load_dwordx4 v151, s[8:11], s14 offen lds
	s_waitcnt vmcnt(8)
	s_waitcnt lgkmcnt(0)
	s_barrier
	s_setprio 1
	s_waitcnt lgkmcnt(6)
	v_mfma_f32_16x16x128_f8f6f4 v[116:119], v[132:139], v[172:179], v[116:119]
	v_mfma_f32_16x16x128_f8f6f4 v[120:123], v[140:147], v[172:179], v[120:123]
	s_waitcnt lgkmcnt(4)
	v_mfma_f32_16x16x128_f8f6f4 v[100:103], v[132:139], v[180:187], v[100:103]
	v_mfma_f32_16x16x128_f8f6f4 v[104:107], v[140:147], v[180:187], v[104:107]
	s_waitcnt lgkmcnt(2)
	v_mfma_f32_16x16x128_f8f6f4 v[208:211], v[132:139], v[188:195], v[84:87]
	v_mfma_f32_16x16x128_f8f6f4 v[212:215], v[140:147], v[188:195], v[88:91]
	s_waitcnt lgkmcnt(0)
	v_mfma_f32_16x16x128_f8f6f4 v[218:221], v[132:139], v[200:207], v[68:71]
	v_mfma_f32_16x16x128_f8f6f4 v[222:225], v[140:147], v[200:207], v[72:75]
	s_setprio 0
	s_setprio 1
	v_mfma_f32_16x16x128_f8f6f4 v[124:127], v[156:163], v[172:179], v[124:127]
	v_mfma_f32_16x16x128_f8f6f4 v[128:131], v[164:171], v[172:179], v[128:131]
	v_mfma_f32_16x16x128_f8f6f4 v[108:111], v[156:163], v[180:187], v[108:111]
	v_mfma_f32_16x16x128_f8f6f4 v[112:115], v[164:171], v[180:187], v[112:115]
	v_mfma_f32_16x16x128_f8f6f4 v[172:175], v[156:163], v[188:195], v[92:95]
	v_mfma_f32_16x16x128_f8f6f4 v[176:179], v[164:171], v[188:195], v[96:99]
	v_mfma_f32_16x16x128_f8f6f4 v[180:183], v[156:163], v[200:207], v[76:79]
	v_mfma_f32_16x16x128_f8f6f4 v[184:187], v[164:171], v[200:207], v[80:83]
	s_setprio 0
	s_barrier
	s_mov_b32 m0, s33
	s_mov_b32 s14, s10
	s_mov_b32 s15, s11
	ds_read_b128 v[68:71], v155 offset:16384
	ds_read_b128 v[72:75], v155 offset:17408
	ds_read_b128 v[76:79], v155 offset:18432
	ds_read_b128 v[80:83], v155 offset:19456
	ds_read_b128 v[84:87], v155 offset:20480
	ds_read_b128 v[88:91], v155 offset:21504
	ds_read_b128 v[92:95], v155 offset:22528
	ds_read_b128 v[96:99], v155 offset:23552
	buffer_load_dwordx4 v150, s[12:15], s76 offen lds
	s_mov_b32 m0, s40
	s_add_i32 s78, s76, 0x2000
	s_and_b64 s[54:55], s[50:51], s[54:55]
	buffer_load_dwordx4 v152, s[12:15], s76 offen lds
	s_mov_b32 m0, s42
	s_and_b64 s[54:55], s[54:55], exec
	buffer_load_dwordx4 v150, s[12:15], s78 offen lds
	s_mov_b32 m0, s43
	s_cselect_b32 s54, s67, s71
	buffer_load_dwordx4 v152, s[12:15], s78 offen lds
	s_add_i32 s54, s77, s54
	s_mov_b32 m0, s29
	s_nop 0
	buffer_load_dwordx4 v149, s[8:11], s54 offen lds
	s_mov_b32 m0, s44
	s_nop 0
	buffer_load_dwordx4 v151, s[8:11], s54 offen lds
	s_waitcnt vmcnt(8)
	s_waitcnt lgkmcnt(0)
	s_barrier
	s_setprio 1
	s_waitcnt lgkmcnt(6)
	v_mfma_f32_16x16x128_f8f6f4 v[52:55], v[132:139], v[68:75], v[52:55]
	v_mfma_f32_16x16x128_f8f6f4 v[56:59], v[140:147], v[68:75], v[56:59]
	s_waitcnt lgkmcnt(4)
	v_mfma_f32_16x16x128_f8f6f4 v[188:191], v[132:139], v[76:83], v[36:39]
	v_mfma_f32_16x16x128_f8f6f4 v[192:195], v[140:147], v[76:83], v[40:43]
	s_waitcnt lgkmcnt(2)
	v_mfma_f32_16x16x128_f8f6f4 v[200:203], v[132:139], v[84:91], v[20:23]
	v_mfma_f32_16x16x128_f8f6f4 v[204:207], v[140:147], v[84:91], v[24:27]
	s_waitcnt lgkmcnt(0)
	v_mfma_f32_16x16x128_f8f6f4 v[226:229], v[132:139], v[92:99], v[4:7]
	v_mfma_f32_16x16x128_f8f6f4 v[230:233], v[140:147], v[92:99], v[8:11]
	s_setprio 0
	s_setprio 1
	v_mfma_f32_16x16x128_f8f6f4 v[60:63], v[156:163], v[68:75], v[60:63]
	v_mfma_f32_16x16x128_f8f6f4 v[64:67], v[164:171], v[68:75], v[64:67]
	v_mfma_f32_16x16x128_f8f6f4 v[234:237], v[156:163], v[76:83], v[44:47]
	v_mfma_f32_16x16x128_f8f6f4 v[238:241], v[164:171], v[76:83], v[48:51]
	v_mfma_f32_16x16x128_f8f6f4 v[242:245], v[156:163], v[84:91], v[28:31]
	v_mfma_f32_16x16x128_f8f6f4 v[246:249], v[164:171], v[84:91], v[32:35]
	v_mfma_f32_16x16x128_f8f6f4 v[250:253], v[156:163], v[92:99], v[12:15]
	v_mfma_f32_16x16x128_f8f6f4 v[196:199], v[164:171], v[92:99], v[16:19]
	s_setprio 0
	s_barrier
	v_add_u32_e32 v1, 0x18000, v154
	ds_read_b128 v[2:5], v1
	ds_read_b128 v[6:9], v1 offset:1024
	s_nop 0
	ds_read_b128 v[10:13], v1 offset:2048
	ds_read_b128 v[14:17], v1 offset:3072
	v_add_u32_e32 v1, 0x1c000, v154
	ds_read_b128 v[132:135], v1
	ds_read_b128 v[136:139], v1 offset:1024
	ds_read_b128 v[140:143], v1 offset:2048
	ds_read_b128 v[144:147], v1 offset:3072
	s_add_i32 s55, s54, 0x20000
	s_mov_b32 m0, s45
	ds_read_b128 v[18:21], v155 offset:32768
	ds_read_b128 v[22:25], v155 offset:33792
	ds_read_b128 v[26:29], v155 offset:34816
	ds_read_b128 v[30:33], v155 offset:35840
	ds_read_b128 v[34:37], v155 offset:36864
	ds_read_b128 v[38:41], v155 offset:37888
	ds_read_b128 v[42:45], v155 offset:38912
	ds_read_b128 v[46:49], v155 offset:39936
	buffer_load_dwordx4 v149, s[8:11], s55 offen lds
	s_mov_b32 m0, s46
	s_nop 0
	buffer_load_dwordx4 v151, s[8:11], s55 offen lds
	s_waitcnt vmcnt(8)
	s_waitcnt lgkmcnt(0)
	s_barrier
	s_setprio 1
	s_waitcnt lgkmcnt(6)
	v_mfma_f32_16x16x128_f8f6f4 v[116:119], v[2:9], v[18:25], v[116:119]
	v_mfma_f32_16x16x128_f8f6f4 v[120:123], v[10:17], v[18:25], v[120:123]
	s_waitcnt lgkmcnt(4)
	v_mfma_f32_16x16x128_f8f6f4 v[100:103], v[2:9], v[26:33], v[100:103]
	v_mfma_f32_16x16x128_f8f6f4 v[104:107], v[10:17], v[26:33], v[104:107]
	s_waitcnt lgkmcnt(2)
	v_mfma_f32_16x16x128_f8f6f4 v[84:87], v[2:9], v[34:41], v[208:211]
	v_mfma_f32_16x16x128_f8f6f4 v[88:91], v[10:17], v[34:41], v[212:215]
	s_waitcnt lgkmcnt(0)
	v_mfma_f32_16x16x128_f8f6f4 v[68:71], v[2:9], v[42:49], v[218:221]
	v_mfma_f32_16x16x128_f8f6f4 v[72:75], v[10:17], v[42:49], v[222:225]
	s_setprio 0
	s_setprio 1
	v_mfma_f32_16x16x128_f8f6f4 v[124:127], v[132:139], v[18:25], v[124:127]
	v_mfma_f32_16x16x128_f8f6f4 v[128:131], v[140:147], v[18:25], v[128:131]
	v_mfma_f32_16x16x128_f8f6f4 v[108:111], v[132:139], v[26:33], v[108:111]
	v_mfma_f32_16x16x128_f8f6f4 v[112:115], v[140:147], v[26:33], v[112:115]
	v_mfma_f32_16x16x128_f8f6f4 v[92:95], v[132:139], v[34:41], v[172:175]
	v_mfma_f32_16x16x128_f8f6f4 v[96:99], v[140:147], v[34:41], v[176:179]
	v_mfma_f32_16x16x128_f8f6f4 v[76:79], v[132:139], v[42:49], v[180:183]
	v_mfma_f32_16x16x128_f8f6f4 v[80:83], v[140:147], v[42:49], v[184:187]
	s_setprio 0
	s_barrier
	s_mov_b32 m0, s47
	s_add_i32 s55, s76, 0x80
	ds_read_b128 v[28:31], v155 offset:49152
	ds_read_b128 v[32:35], v155 offset:50176
	ds_read_b128 v[156:159], v155 offset:51200
	ds_read_b128 v[160:163], v155 offset:52224
	ds_read_b128 v[164:167], v155 offset:53248
	ds_read_b128 v[168:171], v155 offset:54272
	ds_read_b128 v[172:175], v155 offset:55296
	ds_read_b128 v[176:179], v155 offset:56320
	buffer_load_dwordx4 v150, s[12:15], s55 offen lds
	s_mov_b32 m0, s49
	s_addk_i32 s76, 0x2080
	buffer_load_dwordx4 v152, s[12:15], s55 offen lds
	s_mov_b32 m0, s57
	s_addk_i32 s54, 0x80
	buffer_load_dwordx4 v150, s[12:15], s76 offen lds
	s_mov_b32 m0, s58
	s_nop 0
	buffer_load_dwordx4 v152, s[12:15], s76 offen lds
	s_mov_b32 m0, s53
	s_nop 0
	buffer_load_dwordx4 v149, s[8:11], s54 offen lds
	s_mov_b32 m0, s56
	s_nop 0
	buffer_load_dwordx4 v151, s[8:11], s54 offen lds
	s_waitcnt vmcnt(8)
	s_waitcnt lgkmcnt(0)
	s_barrier
	s_setprio 1
	s_waitcnt lgkmcnt(6)
	v_mfma_f32_16x16x128_f8f6f4 v[52:55], v[2:9], v[28:35], v[52:55]
	v_mfma_f32_16x16x128_f8f6f4 v[56:59], v[10:17], v[28:35], v[56:59]
	s_waitcnt lgkmcnt(4)
	v_mfma_f32_16x16x128_f8f6f4 v[36:39], v[2:9], v[156:163], v[188:191]
	v_mfma_f32_16x16x128_f8f6f4 v[40:43], v[10:17], v[156:163], v[192:195]
	s_waitcnt lgkmcnt(2)
	v_mfma_f32_16x16x128_f8f6f4 v[20:23], v[2:9], v[164:171], v[200:203]
	v_mfma_f32_16x16x128_f8f6f4 v[24:27], v[10:17], v[164:171], v[204:207]
	s_waitcnt lgkmcnt(0)
	v_mfma_f32_16x16x128_f8f6f4 v[4:7], v[2:9], v[172:179], v[226:229]
	v_mfma_f32_16x16x128_f8f6f4 v[8:11], v[10:17], v[172:179], v[230:233]
	s_setprio 0
	s_setprio 1
	v_mfma_f32_16x16x128_f8f6f4 v[60:63], v[132:139], v[28:35], v[60:63]
	v_mfma_f32_16x16x128_f8f6f4 v[64:67], v[140:147], v[28:35], v[64:67]
	v_mfma_f32_16x16x128_f8f6f4 v[44:47], v[132:139], v[156:163], v[234:237]
	v_mfma_f32_16x16x128_f8f6f4 v[48:51], v[140:147], v[156:163], v[238:241]
	v_mfma_f32_16x16x128_f8f6f4 v[28:31], v[132:139], v[164:171], v[242:245]
	v_mfma_f32_16x16x128_f8f6f4 v[32:35], v[140:147], v[164:171], v[246:249]
	v_mfma_f32_16x16x128_f8f6f4 v[12:15], v[132:139], v[172:179], v[250:253]
	v_mfma_f32_16x16x128_f8f6f4 v[16:19], v[140:147], v[172:179], v[196:199]
	s_setprio 0
	s_add_i32 s74, s74, 2
	s_addk_i32 s75, 0x100
	s_cmp_gt_u32 s74, 5
	s_barrier
	s_cbranch_scc0 .LBB0_1560
	s_and_b64 vcc, exec, s[26:27]
	s_cbranch_vccz .LBB0_1563
	s_barrier
